# v10
# baseline (speedup 1.0000x reference)
.Lnerf_hid_a0:
	s_waitcnt vmcnt(0) lgkmcnt(0)
	s_barrier
	v_mfma_f32_16x16x32_bf16 v[80:83], v[240:243], v[208:211], v[80:83]
	ds_read_b128 v[224:227], v121 offset:40960
	ds_read_b128 v[228:231], v121 offset:41984
	v_mfma_f32_16x16x32_bf16 v[76:79], v[244:247], v[208:211], v[76:79]
	ds_read_b128 v[232:235], v121 offset:43008
	v_mfma_f32_16x16x32_bf16 v[72:75], v[244:247], v[212:215], v[72:75]
	ds_read_b128 v[236:239], v121 offset:44032
	v_mfma_f32_16x16x32_bf16 v[84:87], v[240:243], v[212:215], v[84:87]
	ds_read_b128 v[240:243], v121 offset:45056
	ds_read_b128 v[244:247], v121 offset:46080
	v_mfma_f32_16x16x32_bf16 v[80:83], v[248:251], v[216:219], v[80:83]
	v_mfma_f32_16x16x32_bf16 v[76:79], v[252:255], v[216:219], v[76:79]
	v_mfma_f32_16x16x32_bf16 v[72:75], v[252:255], v[220:223], v[72:75]
	v_mfma_f32_16x16x32_bf16 v[84:87], v[248:251], v[220:223], v[84:87]
	ds_read_b128 v[248:251], v121 offset:47104
	ds_read_b128 v[252:255], v121 offset:48128
	s_setprio 3
	s_waitcnt lgkmcnt(6)
	v_mfma_f32_16x16x32_bf16 v[64:67], v[224:227], v[0:3], v[152:155]
	v_mfma_f32_16x16x32_bf16 v[68:71], v[228:231], v[0:3], v[156:159]
	v_mfma_f32_16x16x32_bf16 v[60:63], v[228:231], v[4:7], v[156:159]
	v_mfma_f32_16x16x32_bf16 v[56:59], v[224:227], v[4:7], v[152:155]
	ds_read_b128 v[224:227], v121 offset:49152
	ds_read_b128 v[228:231], v121 offset:50176
	s_waitcnt lgkmcnt(6)
	ds_read_b128 v[160:163], v183 offset:128
	ds_read_b128 v[164:167], v183 offset:192
	v_mfma_f32_16x16x32_bf16 v[64:67], v[232:235], v[12:15], v[64:67]
	v_mfma_f32_16x16x32_bf16 v[68:71], v[236:239], v[12:15], v[68:71]
	s_mov_b32 m0, s35
	s_add_i32 s51, s50, 0x0
	v_mfma_f32_16x16x32_bf16 v[60:63], v[236:239], v[8:11], v[60:63]
	buffer_load_dwordx4 v125, s[36:39], s51 offen lds
	v_mfma_f32_16x16x32_bf16 v[56:59], v[232:235], v[8:11], v[56:59]
	ds_read_b128 v[232:235], v121 offset:51200
	ds_read_b128 v[236:239], v121 offset:52224
	s_waitcnt lgkmcnt(8)
	v_mfma_f32_16x16x32_bf16 v[64:67], v[240:243], v[16:19], v[64:67]
	v_mfma_f32_16x16x32_bf16 v[68:71], v[244:247], v[16:19], v[68:71]
	s_mov_b32 m0, s42
	s_add_i32 s51, s50, 0x2000
	v_mfma_f32_16x16x32_bf16 v[60:63], v[244:247], v[20:23], v[60:63]
	buffer_load_dwordx4 v125, s[36:39], s51 offen lds
	v_mfma_f32_16x16x32_bf16 v[56:59], v[240:243], v[20:23], v[56:59]
	ds_read_b128 v[240:243], v121 offset:53248
	ds_read_b128 v[244:247], v121 offset:54272
	s_waitcnt lgkmcnt(8)
	v_mfma_f32_16x16x32_bf16 v[64:67], v[248:251], v[24:27], v[64:67]
	v_cvt_pk_bf16_f32 v112, v80, v81
	v_mfma_f32_16x16x32_bf16 v[68:71], v[252:255], v[24:27], v[68:71]
	s_mov_b32 m0, s41
	s_add_i32 s51, s50, 0x4000
	v_cvt_pk_bf16_f32 v113, v82, v83
	v_mfma_f32_16x16x32_bf16 v[60:63], v[252:255], v[28:31], v[60:63]
	buffer_load_dwordx4 v125, s[36:39], s51 offen lds
	v_cvt_pk_bf16_f32 v114, v76, v77
	v_mfma_f32_16x16x32_bf16 v[56:59], v[248:251], v[28:31], v[56:59]
	v_cvt_pk_bf16_f32 v115, v78, v79
	ds_read_b128 v[248:251], v121 offset:55296
	ds_read_b128 v[252:255], v121 offset:56320
	s_setprio 2
	s_waitcnt lgkmcnt(8)
	v_mfma_f32_16x16x32_bf16 v[64:67], v[224:227], v[32:35], v[64:67]
	v_cvt_pk_bf16_f32 v116, v84, v85
	v_mfma_f32_16x16x32_bf16 v[68:71], v[228:231], v[32:35], v[68:71]
	s_mov_b32 m0, s40
	s_add_i32 s51, s50, 0x6000
	v_cvt_pk_bf16_f32 v117, v86, v87
	v_mfma_f32_16x16x32_bf16 v[60:63], v[228:231], v[36:39], v[60:63]
	buffer_load_dwordx4 v125, s[36:39], s51 offen lds
	v_cvt_pk_bf16_f32 v118, v72, v73
	v_mfma_f32_16x16x32_bf16 v[56:59], v[224:227], v[36:39], v[56:59]
	v_cvt_pk_bf16_f32 v119, v74, v75
	ds_read_b128 v[224:227], v121 offset:57344
	ds_read_b128 v[228:231], v121 offset:58368
	s_waitcnt lgkmcnt(6)
	v_mfma_f32_16x16x32_bf16 v[64:67], v[232:235], v[40:43], v[64:67]
	v_pk_max_i16 v112, v112, 0
	v_mfma_f32_16x16x32_bf16 v[68:71], v[236:239], v[40:43], v[68:71]
	v_pk_max_i16 v113, v113, 0
	v_mfma_f32_16x16x32_bf16 v[60:63], v[236:239], v[44:47], v[60:63]
	v_pk_max_i16 v114, v114, 0
	v_mfma_f32_16x16x32_bf16 v[56:59], v[232:235], v[44:47], v[56:59]
	v_pk_max_i16 v115, v115, 0
	ds_read_b128 v[232:235], v121 offset:59392
	ds_read_b128 v[236:239], v121 offset:60416
	s_waitcnt lgkmcnt(6)
	ds_read_b128 v[152:155], v183 offset:256
	ds_read_b128 v[156:159], v183 offset:320
	v_mfma_f32_16x16x32_bf16 v[64:67], v[240:243], v[48:51], v[64:67]
	v_pk_max_i16 v116, v116, 0
	v_mfma_f32_16x16x32_bf16 v[68:71], v[244:247], v[48:51], v[68:71]
	v_pk_max_i16 v117, v117, 0
	v_mfma_f32_16x16x32_bf16 v[60:63], v[244:247], v[52:55], v[60:63]
	v_pk_max_i16 v118, v118, 0
	v_mfma_f32_16x16x32_bf16 v[56:59], v[240:243], v[52:55], v[56:59]
	v_pk_max_i16 v119, v119, 0
	ds_read_b128 v[240:243], v121 offset:61440
	ds_read_b128 v[244:247], v121 offset:62464
	s_waitcnt lgkmcnt(8)
	v_mfma_f32_16x16x32_bf16 v[64:67], v[248:251], v[112:115], v[64:67]
	v_mfma_f32_16x16x32_bf16 v[68:71], v[252:255], v[112:115], v[68:71]
	v_mfma_f32_16x16x32_bf16 v[60:63], v[252:255], v[116:119], v[60:63]
	v_mfma_f32_16x16x32_bf16 v[56:59], v[248:251], v[116:119], v[56:59]
	ds_read_b128 v[248:251], v121 offset:63488
	ds_read_b128 v[252:255], v121 offset:64512
	s_setprio 1
	s_waitcnt lgkmcnt(8)
	v_mfma_f32_16x16x32_bf16 v[80:83], v[224:227], v[0:3], v[160:163]
	v_mfma_f32_16x16x32_bf16 v[76:79], v[228:231], v[0:3], v[164:167]
	v_mfma_f32_16x16x32_bf16 v[72:75], v[228:231], v[4:7], v[164:167]
	v_mfma_f32_16x16x32_bf16 v[84:87], v[224:227], v[4:7], v[160:163]
	ds_read_b128 v[224:227], v126 offset:57344
	ds_read_b128 v[228:231], v126 offset:58368
	s_waitcnt lgkmcnt(8)
	v_mfma_f32_16x16x32_bf16 v[80:83], v[232:235], v[12:15], v[80:83]
	v_cvt_pk_bf16_f32 v88, v64, v65
	v_mfma_f32_16x16x32_bf16 v[76:79], v[236:239], v[12:15], v[76:79]
	v_cvt_pk_bf16_f32 v89, v66, v67
	v_mfma_f32_16x16x32_bf16 v[72:75], v[236:239], v[8:11], v[72:75]
	v_cvt_pk_bf16_f32 v90, v68, v69
	v_mfma_f32_16x16x32_bf16 v[84:87], v[232:235], v[8:11], v[84:87]
	v_cvt_pk_bf16_f32 v91, v70, v71
	ds_read_b128 v[232:235], v126 offset:59392
	ds_read_b128 v[236:239], v126 offset:60416
	s_waitcnt lgkmcnt(6)
	v_mfma_f32_16x16x32_bf16 v[80:83], v[240:243], v[16:19], v[80:83]
	v_cvt_pk_bf16_f32 v92, v56, v57
	v_mfma_f32_16x16x32_bf16 v[76:79], v[244:247], v[16:19], v[76:79]
	v_cvt_pk_bf16_f32 v93, v58, v59
	v_mfma_f32_16x16x32_bf16 v[72:75], v[244:247], v[20:23], v[72:75]
	v_cvt_pk_bf16_f32 v94, v60, v61
	v_mfma_f32_16x16x32_bf16 v[84:87], v[240:243], v[20:23], v[84:87]
	v_cvt_pk_bf16_f32 v95, v62, v63
	ds_read_b128 v[240:243], v126 offset:61440
	ds_read_b128 v[244:247], v126 offset:62464
	s_waitcnt lgkmcnt(6)
	v_mfma_f32_16x16x32_bf16 v[80:83], v[248:251], v[24:27], v[80:83]
	v_pk_max_i16 v88, v88, 0
	v_mfma_f32_16x16x32_bf16 v[76:79], v[252:255], v[24:27], v[76:79]
	v_pk_max_i16 v89, v89, 0
	v_mfma_f32_16x16x32_bf16 v[72:75], v[252:255], v[28:31], v[72:75]
	v_pk_max_i16 v90, v90, 0
	v_mfma_f32_16x16x32_bf16 v[84:87], v[248:251], v[28:31], v[84:87]
	v_pk_max_i16 v91, v91, 0
	ds_read_b128 v[248:251], v126 offset:63488
	ds_read_b128 v[252:255], v126 offset:64512
	s_setprio 0
	s_waitcnt lgkmcnt(6)
	v_mfma_f32_16x16x32_bf16 v[80:83], v[224:227], v[32:35], v[80:83]
	v_pk_max_i16 v92, v92, 0
	v_mfma_f32_16x16x32_bf16 v[76:79], v[228:231], v[32:35], v[76:79]
	v_pk_max_i16 v93, v93, 0
	v_mfma_f32_16x16x32_bf16 v[72:75], v[228:231], v[36:39], v[72:75]
	v_pk_max_i16 v94, v94, 0
	v_mfma_f32_16x16x32_bf16 v[84:87], v[224:227], v[36:39], v[84:87]
	v_pk_max_i16 v95, v95, 0
	s_waitcnt lgkmcnt(4)
	v_mfma_f32_16x16x32_bf16 v[80:83], v[232:235], v[40:43], v[80:83]
	v_mfma_f32_16x16x32_bf16 v[76:79], v[236:239], v[40:43], v[76:79]
	v_mfma_f32_16x16x32_bf16 v[72:75], v[236:239], v[44:47], v[72:75]
	v_mfma_f32_16x16x32_bf16 v[84:87], v[232:235], v[44:47], v[84:87]
.Lnerf_hid_a1:
	s_waitcnt vmcnt(0) lgkmcnt(0)
	s_barrier
	v_mfma_f32_16x16x32_bf16 v[80:83], v[240:243], v[48:51], v[80:83]
	ds_read_b128 v[224:227], v121 offset:8192
	ds_read_b128 v[228:231], v121 offset:9216
	v_mfma_f32_16x16x32_bf16 v[76:79], v[244:247], v[48:51], v[76:79]
	ds_read_b128 v[232:235], v121 offset:10240
	v_mfma_f32_16x16x32_bf16 v[72:75], v[244:247], v[52:55], v[72:75]
	ds_read_b128 v[236:239], v121 offset:11264
	v_mfma_f32_16x16x32_bf16 v[84:87], v[240:243], v[52:55], v[84:87]
	ds_read_b128 v[240:243], v121 offset:12288
	ds_read_b128 v[244:247], v121 offset:13312
	v_mfma_f32_16x16x32_bf16 v[80:83], v[248:251], v[112:115], v[80:83]
	v_mfma_f32_16x16x32_bf16 v[76:79], v[252:255], v[112:115], v[76:79]
	v_mfma_f32_16x16x32_bf16 v[72:75], v[252:255], v[116:119], v[72:75]
	v_mfma_f32_16x16x32_bf16 v[84:87], v[248:251], v[116:119], v[84:87]
	ds_read_b128 v[248:251], v121 offset:14336
	ds_read_b128 v[252:255], v121 offset:15360
	s_setprio 3
	s_waitcnt lgkmcnt(6)
	v_mfma_f32_16x16x32_bf16 v[64:67], v[224:227], v[0:3], v[152:155]
	v_mfma_f32_16x16x32_bf16 v[68:71], v[228:231], v[0:3], v[156:159]
	v_mfma_f32_16x16x32_bf16 v[60:63], v[228:231], v[4:7], v[156:159]
	v_mfma_f32_16x16x32_bf16 v[56:59], v[224:227], v[4:7], v[152:155]
	ds_read_b128 v[224:227], v121 offset:16384
	ds_read_b128 v[228:231], v121 offset:17408
	s_waitcnt lgkmcnt(6)
	ds_read_b128 v[160:163], v183 offset:384
	ds_read_b128 v[164:167], v183 offset:448
	v_mfma_f32_16x16x32_bf16 v[64:67], v[232:235], v[12:15], v[64:67]
	v_mfma_f32_16x16x32_bf16 v[68:71], v[236:239], v[12:15], v[68:71]
	s_mov_b32 m0, s28
	s_add_i32 s51, s50, 0x8000
	v_mfma_f32_16x16x32_bf16 v[60:63], v[236:239], v[8:11], v[60:63]
	buffer_load_dwordx4 v125, s[36:39], s51 offen lds
	v_mfma_f32_16x16x32_bf16 v[56:59], v[232:235], v[8:11], v[56:59]
	ds_read_b128 v[232:235], v121 offset:18432
	ds_read_b128 v[236:239], v121 offset:19456
	s_waitcnt lgkmcnt(8)
	v_mfma_f32_16x16x32_bf16 v[64:67], v[240:243], v[16:19], v[64:67]
	v_mfma_f32_16x16x32_bf16 v[68:71], v[244:247], v[16:19], v[68:71]
	s_mov_b32 m0, s29
	s_add_i32 s51, s50, 0xa000
	v_mfma_f32_16x16x32_bf16 v[60:63], v[244:247], v[20:23], v[60:63]
	buffer_load_dwordx4 v125, s[36:39], s51 offen lds
	v_mfma_f32_16x16x32_bf16 v[56:59], v[240:243], v[20:23], v[56:59]
	ds_read_b128 v[240:243], v121 offset:20480
	ds_read_b128 v[244:247], v121 offset:21504
	s_waitcnt lgkmcnt(8)
	v_mfma_f32_16x16x32_bf16 v[64:67], v[248:251], v[24:27], v[64:67]
	v_mfma_f32_16x16x32_bf16 v[68:71], v[252:255], v[24:27], v[68:71]
	s_mov_b32 m0, s33
	s_add_i32 s51, s50, 0xc000
	v_mfma_f32_16x16x32_bf16 v[60:63], v[252:255], v[28:31], v[60:63]
	buffer_load_dwordx4 v125, s[36:39], s51 offen lds
	v_mfma_f32_16x16x32_bf16 v[56:59], v[248:251], v[28:31], v[56:59]
	ds_read_b128 v[248:251], v121 offset:22528
	ds_read_b128 v[252:255], v121 offset:23552
	s_setprio 2
	s_waitcnt lgkmcnt(8)
	v_mfma_f32_16x16x32_bf16 v[64:67], v[224:227], v[32:35], v[64:67]
	v_mfma_f32_16x16x32_bf16 v[68:71], v[228:231], v[32:35], v[68:71]
	s_mov_b32 m0, s34
	s_add_i32 s51, s50, 0xe000
	v_mfma_f32_16x16x32_bf16 v[60:63], v[228:231], v[36:39], v[60:63]
	buffer_load_dwordx4 v125, s[36:39], s51 offen lds
	v_mfma_f32_16x16x32_bf16 v[56:59], v[224:227], v[36:39], v[56:59]
	ds_read_b128 v[224:227], v121 offset:24576
	ds_read_b128 v[228:231], v121 offset:25600
	s_waitcnt lgkmcnt(6)
	v_mfma_f32_16x16x32_bf16 v[64:67], v[232:235], v[40:43], v[64:67]
	v_cvt_pk_bf16_f32 v96, v80, v81
	v_mfma_f32_16x16x32_bf16 v[68:71], v[236:239], v[40:43], v[68:71]
	v_cvt_pk_bf16_f32 v97, v82, v83
	v_mfma_f32_16x16x32_bf16 v[60:63], v[236:239], v[44:47], v[60:63]
	v_cvt_pk_bf16_f32 v98, v76, v77
	v_mfma_f32_16x16x32_bf16 v[56:59], v[232:235], v[44:47], v[56:59]
	v_cvt_pk_bf16_f32 v99, v78, v79
	ds_read_b128 v[232:235], v121 offset:26624
	ds_read_b128 v[236:239], v121 offset:27648
	s_waitcnt lgkmcnt(6)
	ds_read_b128 v[152:155], v183 offset:512
	ds_read_b128 v[156:159], v183 offset:576
	v_mfma_f32_16x16x32_bf16 v[64:67], v[240:243], v[48:51], v[64:67]
	v_cvt_pk_bf16_f32 v100, v84, v85
	v_mfma_f32_16x16x32_bf16 v[68:71], v[244:247], v[48:51], v[68:71]
	v_cvt_pk_bf16_f32 v101, v86, v87
	v_mfma_f32_16x16x32_bf16 v[60:63], v[244:247], v[52:55], v[60:63]
	v_cvt_pk_bf16_f32 v102, v72, v73
	v_mfma_f32_16x16x32_bf16 v[56:59], v[240:243], v[52:55], v[56:59]
	v_cvt_pk_bf16_f32 v103, v74, v75
	ds_read_b128 v[240:243], v121 offset:28672
	ds_read_b128 v[244:247], v121 offset:29696
	s_waitcnt lgkmcnt(8)
	v_mfma_f32_16x16x32_bf16 v[64:67], v[248:251], v[112:115], v[64:67]
	v_pk_max_i16 v96, v96, 0
	v_mfma_f32_16x16x32_bf16 v[68:71], v[252:255], v[112:115], v[68:71]
	v_pk_max_i16 v97, v97, 0
	v_mfma_f32_16x16x32_bf16 v[60:63], v[252:255], v[116:119], v[60:63]
	v_pk_max_i16 v98, v98, 0
	v_mfma_f32_16x16x32_bf16 v[56:59], v[248:251], v[116:119], v[56:59]
	v_pk_max_i16 v99, v99, 0
	ds_read_b128 v[248:251], v121 offset:30720
	ds_read_b128 v[252:255], v121 offset:31744
	s_setprio 1
	s_waitcnt lgkmcnt(8)
	v_mfma_f32_16x16x32_bf16 v[80:83], v[224:227], v[0:3], v[160:163]
	v_pk_max_i16 v100, v100, 0
	v_mfma_f32_16x16x32_bf16 v[76:79], v[228:231], v[0:3], v[164:167]
	v_pk_max_i16 v101, v101, 0
	v_mfma_f32_16x16x32_bf16 v[72:75], v[228:231], v[4:7], v[164:167]
	v_pk_max_i16 v102, v102, 0
	v_mfma_f32_16x16x32_bf16 v[84:87], v[224:227], v[4:7], v[160:163]
	v_pk_max_i16 v103, v103, 0
	ds_read_b128 v[224:227], v121 offset:32768
	ds_read_b128 v[228:231], v121 offset:33792
	s_waitcnt lgkmcnt(8)
	v_mfma_f32_16x16x32_bf16 v[80:83], v[232:235], v[12:15], v[80:83]
	v_cvt_pk_bf16_f32 v104, v64, v65
	v_mfma_f32_16x16x32_bf16 v[76:79], v[236:239], v[12:15], v[76:79]
	v_cvt_pk_bf16_f32 v105, v66, v67
	v_mfma_f32_16x16x32_bf16 v[72:75], v[236:239], v[8:11], v[72:75]
	v_cvt_pk_bf16_f32 v106, v68, v69
	v_mfma_f32_16x16x32_bf16 v[84:87], v[232:235], v[8:11], v[84:87]
	v_cvt_pk_bf16_f32 v107, v70, v71
	ds_read_b128 v[232:235], v121 offset:34816
	ds_read_b128 v[236:239], v121 offset:35840
	s_waitcnt lgkmcnt(6)
	v_mfma_f32_16x16x32_bf16 v[80:83], v[240:243], v[16:19], v[80:83]
	v_cvt_pk_bf16_f32 v108, v56, v57
	v_mfma_f32_16x16x32_bf16 v[76:79], v[244:247], v[16:19], v[76:79]
	v_cvt_pk_bf16_f32 v109, v58, v59
	v_mfma_f32_16x16x32_bf16 v[72:75], v[244:247], v[20:23], v[72:75]
	v_cvt_pk_bf16_f32 v110, v60, v61
	v_mfma_f32_16x16x32_bf16 v[84:87], v[240:243], v[20:23], v[84:87]
	v_cvt_pk_bf16_f32 v111, v62, v63
	ds_read_b128 v[240:243], v121 offset:36864
	ds_read_b128 v[244:247], v121 offset:37888
	s_waitcnt lgkmcnt(6)
	v_mfma_f32_16x16x32_bf16 v[80:83], v[248:251], v[24:27], v[80:83]
	v_pk_max_i16 v104, v104, 0
	v_mfma_f32_16x16x32_bf16 v[76:79], v[252:255], v[24:27], v[76:79]
	v_pk_max_i16 v105, v105, 0
	v_mfma_f32_16x16x32_bf16 v[72:75], v[252:255], v[28:31], v[72:75]
	v_pk_max_i16 v106, v106, 0
	v_mfma_f32_16x16x32_bf16 v[84:87], v[248:251], v[28:31], v[84:87]
	v_pk_max_i16 v107, v107, 0
	ds_read_b128 v[248:251], v121 offset:38912
	ds_read_b128 v[252:255], v121 offset:39936
	s_setprio 0
	s_waitcnt lgkmcnt(6)
	v_mfma_f32_16x16x32_bf16 v[80:83], v[224:227], v[32:35], v[80:83]
	v_pk_max_i16 v108, v108, 0
	v_mfma_f32_16x16x32_bf16 v[76:79], v[228:231], v[32:35], v[76:79]
	v_pk_max_i16 v109, v109, 0
	v_mfma_f32_16x16x32_bf16 v[72:75], v[228:231], v[36:39], v[72:75]
	v_pk_max_i16 v110, v110, 0
	v_mfma_f32_16x16x32_bf16 v[84:87], v[224:227], v[36:39], v[84:87]
	v_pk_max_i16 v111, v111, 0
	s_waitcnt lgkmcnt(4)
	v_mfma_f32_16x16x32_bf16 v[80:83], v[232:235], v[40:43], v[80:83]
	v_mfma_f32_16x16x32_bf16 v[76:79], v[236:239], v[40:43], v[76:79]
	v_mfma_f32_16x16x32_bf16 v[72:75], v[236:239], v[44:47], v[72:75]
	v_mfma_f32_16x16x32_bf16 v[84:87], v[232:235], v[44:47], v[84:87]
.Lnerf_hid_a2:
	s_waitcnt vmcnt(0) lgkmcnt(0)
	s_barrier
	v_mfma_f32_16x16x32_bf16 v[80:83], v[240:243], v[48:51], v[80:83]
	ds_read_b128 v[224:227], v121 offset:40960
	ds_read_b128 v[228:231], v121 offset:41984
	v_mfma_f32_16x16x32_bf16 v[76:79], v[244:247], v[48:51], v[76:79]
	ds_read_b128 v[232:235], v121 offset:43008
	v_mfma_f32_16x16x32_bf16 v[72:75], v[244:247], v[52:55], v[72:75]
	ds_read_b128 v[236:239], v121 offset:44032
	v_mfma_f32_16x16x32_bf16 v[84:87], v[240:243], v[52:55], v[84:87]
	ds_read_b128 v[240:243], v121 offset:45056
	ds_read_b128 v[244:247], v121 offset:46080
	v_mfma_f32_16x16x32_bf16 v[80:83], v[248:251], v[112:115], v[80:83]
	v_mfma_f32_16x16x32_bf16 v[76:79], v[252:255], v[112:115], v[76:79]
	v_mfma_f32_16x16x32_bf16 v[72:75], v[252:255], v[116:119], v[72:75]
	v_mfma_f32_16x16x32_bf16 v[84:87], v[248:251], v[116:119], v[84:87]
	ds_read_b128 v[248:251], v121 offset:47104
	ds_read_b128 v[252:255], v121 offset:48128
	s_setprio 3
	s_waitcnt lgkmcnt(6)
	v_mfma_f32_16x16x32_bf16 v[64:67], v[224:227], v[0:3], v[152:155]
	v_mfma_f32_16x16x32_bf16 v[68:71], v[228:231], v[0:3], v[156:159]
	v_mfma_f32_16x16x32_bf16 v[60:63], v[228:231], v[4:7], v[156:159]
	v_mfma_f32_16x16x32_bf16 v[56:59], v[224:227], v[4:7], v[152:155]
	ds_read_b128 v[224:227], v121 offset:49152
	ds_read_b128 v[228:231], v121 offset:50176
	s_waitcnt lgkmcnt(6)
	ds_read_b128 v[160:163], v183 offset:640
	ds_read_b128 v[164:167], v183 offset:704
	v_mfma_f32_16x16x32_bf16 v[64:67], v[232:235], v[12:15], v[64:67]
	v_mfma_f32_16x16x32_bf16 v[68:71], v[236:239], v[12:15], v[68:71]
	s_mov_b32 m0, s35
	s_add_i32 s51, s50, 0x10000
	v_mfma_f32_16x16x32_bf16 v[60:63], v[236:239], v[8:11], v[60:63]
	buffer_load_dwordx4 v125, s[36:39], s51 offen lds
	v_mfma_f32_16x16x32_bf16 v[56:59], v[232:235], v[8:11], v[56:59]
	ds_read_b128 v[232:235], v121 offset:51200
	ds_read_b128 v[236:239], v121 offset:52224
	s_waitcnt lgkmcnt(8)
	v_mfma_f32_16x16x32_bf16 v[64:67], v[240:243], v[16:19], v[64:67]
	v_mfma_f32_16x16x32_bf16 v[68:71], v[244:247], v[16:19], v[68:71]
	s_mov_b32 m0, s42
	s_add_i32 s51, s50, 0x12000
	v_mfma_f32_16x16x32_bf16 v[60:63], v[244:247], v[20:23], v[60:63]
	buffer_load_dwordx4 v125, s[36:39], s51 offen lds
	v_mfma_f32_16x16x32_bf16 v[56:59], v[240:243], v[20:23], v[56:59]
	ds_read_b128 v[240:243], v121 offset:53248
	ds_read_b128 v[244:247], v121 offset:54272
	s_waitcnt lgkmcnt(8)
	v_mfma_f32_16x16x32_bf16 v[64:67], v[248:251], v[24:27], v[64:67]
	v_mfma_f32_16x16x32_bf16 v[68:71], v[252:255], v[24:27], v[68:71]
	s_mov_b32 m0, s41
	s_add_i32 s51, s50, 0x14000
	v_mfma_f32_16x16x32_bf16 v[60:63], v[252:255], v[28:31], v[60:63]
	buffer_load_dwordx4 v125, s[36:39], s51 offen lds
	v_mfma_f32_16x16x32_bf16 v[56:59], v[248:251], v[28:31], v[56:59]
	ds_read_b128 v[248:251], v121 offset:55296
	ds_read_b128 v[252:255], v121 offset:56320
	s_setprio 2
	s_waitcnt lgkmcnt(8)
	v_mfma_f32_16x16x32_bf16 v[64:67], v[224:227], v[32:35], v[64:67]
	v_mfma_f32_16x16x32_bf16 v[68:71], v[228:231], v[32:35], v[68:71]
	s_mov_b32 m0, s40
	s_add_i32 s51, s50, 0x16000
	v_mfma_f32_16x16x32_bf16 v[60:63], v[228:231], v[36:39], v[60:63]
	buffer_load_dwordx4 v125, s[36:39], s51 offen lds
	v_mfma_f32_16x16x32_bf16 v[56:59], v[224:227], v[36:39], v[56:59]
	ds_read_b128 v[224:227], v121 offset:57344
	ds_read_b128 v[228:231], v121 offset:58368
	s_waitcnt lgkmcnt(6)
	v_mfma_f32_16x16x32_bf16 v[64:67], v[232:235], v[40:43], v[64:67]
	v_cvt_pk_bf16_f32 v184, v80, v81
	v_mfma_f32_16x16x32_bf16 v[68:71], v[236:239], v[40:43], v[68:71]
	v_cvt_pk_bf16_f32 v185, v82, v83
	v_mfma_f32_16x16x32_bf16 v[60:63], v[236:239], v[44:47], v[60:63]
	v_cvt_pk_bf16_f32 v186, v76, v77
	v_mfma_f32_16x16x32_bf16 v[56:59], v[232:235], v[44:47], v[56:59]
	v_cvt_pk_bf16_f32 v187, v78, v79
	ds_read_b128 v[232:235], v121 offset:59392
	ds_read_b128 v[236:239], v121 offset:60416
	s_waitcnt lgkmcnt(6)
	ds_read_b128 v[152:155], v183 offset:768
	ds_read_b128 v[156:159], v183 offset:832
	v_mfma_f32_16x16x32_bf16 v[64:67], v[240:243], v[48:51], v[64:67]
	v_cvt_pk_bf16_f32 v188, v84, v85
	v_mfma_f32_16x16x32_bf16 v[68:71], v[244:247], v[48:51], v[68:71]
	v_cvt_pk_bf16_f32 v189, v86, v87
	v_mfma_f32_16x16x32_bf16 v[60:63], v[244:247], v[52:55], v[60:63]
	v_cvt_pk_bf16_f32 v190, v72, v73
	v_mfma_f32_16x16x32_bf16 v[56:59], v[240:243], v[52:55], v[56:59]
	v_cvt_pk_bf16_f32 v191, v74, v75
	ds_read_b128 v[240:243], v121 offset:61440
	ds_read_b128 v[244:247], v121 offset:62464
	s_waitcnt lgkmcnt(8)
	v_mfma_f32_16x16x32_bf16 v[64:67], v[248:251], v[112:115], v[64:67]
	v_pk_max_i16 v184, v184, 0
	v_mfma_f32_16x16x32_bf16 v[68:71], v[252:255], v[112:115], v[68:71]
	v_pk_max_i16 v185, v185, 0
	v_mfma_f32_16x16x32_bf16 v[60:63], v[252:255], v[116:119], v[60:63]
	v_pk_max_i16 v186, v186, 0
	v_mfma_f32_16x16x32_bf16 v[56:59], v[248:251], v[116:119], v[56:59]
	v_pk_max_i16 v187, v187, 0
	ds_read_b128 v[248:251], v121 offset:63488
	ds_read_b128 v[252:255], v121 offset:64512
	s_setprio 1
	s_waitcnt lgkmcnt(8)
	v_mfma_f32_16x16x32_bf16 v[80:83], v[224:227], v[0:3], v[160:163]
	v_pk_max_i16 v188, v188, 0
	v_mfma_f32_16x16x32_bf16 v[76:79], v[228:231], v[0:3], v[164:167]
	v_pk_max_i16 v189, v189, 0
	v_mfma_f32_16x16x32_bf16 v[72:75], v[228:231], v[4:7], v[164:167]
	v_pk_max_i16 v190, v190, 0
	v_mfma_f32_16x16x32_bf16 v[84:87], v[224:227], v[4:7], v[160:163]
	v_pk_max_i16 v191, v191, 0
	ds_read_b128 v[224:227], v126 offset:57344
	ds_read_b128 v[228:231], v126 offset:58368
	s_waitcnt lgkmcnt(8)
	v_mfma_f32_16x16x32_bf16 v[80:83], v[232:235], v[12:15], v[80:83]
	v_cvt_pk_bf16_f32 v192, v64, v65
	v_mfma_f32_16x16x32_bf16 v[76:79], v[236:239], v[12:15], v[76:79]
	v_cvt_pk_bf16_f32 v193, v66, v67
	v_mfma_f32_16x16x32_bf16 v[72:75], v[236:239], v[8:11], v[72:75]
	v_cvt_pk_bf16_f32 v194, v68, v69
	v_mfma_f32_16x16x32_bf16 v[84:87], v[232:235], v[8:11], v[84:87]
	v_cvt_pk_bf16_f32 v195, v70, v71
	ds_read_b128 v[232:235], v126 offset:59392
	ds_read_b128 v[236:239], v126 offset:60416
	s_waitcnt lgkmcnt(6)
	v_mfma_f32_16x16x32_bf16 v[80:83], v[240:243], v[16:19], v[80:83]
	v_cvt_pk_bf16_f32 v196, v56, v57
	v_mfma_f32_16x16x32_bf16 v[76:79], v[244:247], v[16:19], v[76:79]
	v_cvt_pk_bf16_f32 v197, v58, v59
	v_mfma_f32_16x16x32_bf16 v[72:75], v[244:247], v[20:23], v[72:75]
	v_cvt_pk_bf16_f32 v198, v60, v61
	v_mfma_f32_16x16x32_bf16 v[84:87], v[240:243], v[20:23], v[84:87]
	v_cvt_pk_bf16_f32 v199, v62, v63
	ds_read_b128 v[240:243], v126 offset:61440
	ds_read_b128 v[244:247], v126 offset:62464
	s_waitcnt lgkmcnt(6)
	v_mfma_f32_16x16x32_bf16 v[80:83], v[248:251], v[24:27], v[80:83]
	v_pk_max_i16 v192, v192, 0
	v_mfma_f32_16x16x32_bf16 v[76:79], v[252:255], v[24:27], v[76:79]
	v_pk_max_i16 v193, v193, 0
	v_mfma_f32_16x16x32_bf16 v[72:75], v[252:255], v[28:31], v[72:75]
	v_pk_max_i16 v194, v194, 0
	v_mfma_f32_16x16x32_bf16 v[84:87], v[248:251], v[28:31], v[84:87]
	v_pk_max_i16 v195, v195, 0
	ds_read_b128 v[248:251], v126 offset:63488
	ds_read_b128 v[252:255], v126 offset:64512
	s_setprio 0
	s_waitcnt lgkmcnt(6)
	v_mfma_f32_16x16x32_bf16 v[80:83], v[224:227], v[32:35], v[80:83]
	v_pk_max_i16 v196, v196, 0
	v_mfma_f32_16x16x32_bf16 v[76:79], v[228:231], v[32:35], v[76:79]
	v_pk_max_i16 v197, v197, 0
	v_mfma_f32_16x16x32_bf16 v[72:75], v[228:231], v[36:39], v[72:75]
	v_pk_max_i16 v198, v198, 0
	v_mfma_f32_16x16x32_bf16 v[84:87], v[224:227], v[36:39], v[84:87]
	v_pk_max_i16 v199, v199, 0
	s_waitcnt lgkmcnt(4)
	v_mfma_f32_16x16x32_bf16 v[80:83], v[232:235], v[40:43], v[80:83]
	v_mfma_f32_16x16x32_bf16 v[76:79], v[236:239], v[40:43], v[76:79]
	v_mfma_f32_16x16x32_bf16 v[72:75], v[236:239], v[44:47], v[72:75]
	v_mfma_f32_16x16x32_bf16 v[84:87], v[232:235], v[44:47], v[84:87]
.Lnerf_hid_a3:
	s_waitcnt vmcnt(0) lgkmcnt(0)
	s_barrier
	v_mfma_f32_16x16x32_bf16 v[80:83], v[240:243], v[48:51], v[80:83]
	ds_read_b128 v[224:227], v121 offset:8192
	ds_read_b128 v[228:231], v121 offset:9216
	v_mfma_f32_16x16x32_bf16 v[76:79], v[244:247], v[48:51], v[76:79]
	ds_read_b128 v[232:235], v121 offset:10240
	v_mfma_f32_16x16x32_bf16 v[72:75], v[244:247], v[52:55], v[72:75]
	ds_read_b128 v[236:239], v121 offset:11264
	v_mfma_f32_16x16x32_bf16 v[84:87], v[240:243], v[52:55], v[84:87]
	ds_read_b128 v[240:243], v121 offset:12288
	ds_read_b128 v[244:247], v121 offset:13312
	v_mfma_f32_16x16x32_bf16 v[80:83], v[248:251], v[112:115], v[80:83]
	v_mfma_f32_16x16x32_bf16 v[76:79], v[252:255], v[112:115], v[76:79]
	v_mfma_f32_16x16x32_bf16 v[72:75], v[252:255], v[116:119], v[72:75]
	v_mfma_f32_16x16x32_bf16 v[84:87], v[248:251], v[116:119], v[84:87]
	ds_read_b128 v[248:251], v121 offset:14336
	ds_read_b128 v[252:255], v121 offset:15360
	s_setprio 3
	s_waitcnt lgkmcnt(6)
	v_mfma_f32_16x16x32_bf16 v[64:67], v[224:227], v[0:3], v[152:155]
	v_mfma_f32_16x16x32_bf16 v[68:71], v[228:231], v[0:3], v[156:159]
	v_mfma_f32_16x16x32_bf16 v[60:63], v[228:231], v[4:7], v[156:159]
	v_mfma_f32_16x16x32_bf16 v[56:59], v[224:227], v[4:7], v[152:155]
	ds_read_b128 v[224:227], v121 offset:16384
	ds_read_b128 v[228:231], v121 offset:17408
	s_waitcnt lgkmcnt(6)
	ds_read_b128 v[160:163], v183 offset:896
	ds_read_b128 v[164:167], v183 offset:960
	v_mfma_f32_16x16x32_bf16 v[64:67], v[232:235], v[12:15], v[64:67]
	v_mfma_f32_16x16x32_bf16 v[68:71], v[236:239], v[12:15], v[68:71]
	s_mov_b32 m0, s28
	s_add_i32 s51, s50, 0x18000
	v_mfma_f32_16x16x32_bf16 v[60:63], v[236:239], v[8:11], v[60:63]
	buffer_load_dwordx4 v125, s[36:39], s51 offen lds
	v_mfma_f32_16x16x32_bf16 v[56:59], v[232:235], v[8:11], v[56:59]
	ds_read_b128 v[232:235], v121 offset:18432
	ds_read_b128 v[236:239], v121 offset:19456
	s_waitcnt lgkmcnt(8)
	v_mfma_f32_16x16x32_bf16 v[64:67], v[240:243], v[16:19], v[64:67]
	v_mfma_f32_16x16x32_bf16 v[68:71], v[244:247], v[16:19], v[68:71]
	s_mov_b32 m0, s29
	s_add_i32 s51, s50, 0x1a000
	v_mfma_f32_16x16x32_bf16 v[60:63], v[244:247], v[20:23], v[60:63]
	buffer_load_dwordx4 v125, s[36:39], s51 offen lds
	v_mfma_f32_16x16x32_bf16 v[56:59], v[240:243], v[20:23], v[56:59]
	ds_read_b128 v[240:243], v121 offset:20480
	ds_read_b128 v[244:247], v121 offset:21504
	s_waitcnt lgkmcnt(8)
	v_mfma_f32_16x16x32_bf16 v[64:67], v[248:251], v[24:27], v[64:67]
	v_mfma_f32_16x16x32_bf16 v[68:71], v[252:255], v[24:27], v[68:71]
	s_mov_b32 m0, s33
	s_add_i32 s51, s50, 0x1c000
	v_mfma_f32_16x16x32_bf16 v[60:63], v[252:255], v[28:31], v[60:63]
	buffer_load_dwordx4 v125, s[36:39], s51 offen lds
	v_mfma_f32_16x16x32_bf16 v[56:59], v[248:251], v[28:31], v[56:59]
	ds_read_b128 v[248:251], v121 offset:22528
	ds_read_b128 v[252:255], v121 offset:23552
	s_setprio 2
	s_waitcnt lgkmcnt(8)
	v_mfma_f32_16x16x32_bf16 v[64:67], v[224:227], v[32:35], v[64:67]
	v_mfma_f32_16x16x32_bf16 v[68:71], v[228:231], v[32:35], v[68:71]
	s_mov_b32 m0, s34
	s_add_i32 s51, s50, 0x1e000
	v_mfma_f32_16x16x32_bf16 v[60:63], v[228:231], v[36:39], v[60:63]
	buffer_load_dwordx4 v125, s[36:39], s51 offen lds
	v_mfma_f32_16x16x32_bf16 v[56:59], v[224:227], v[36:39], v[56:59]
	ds_read_b128 v[224:227], v121 offset:24576
	ds_read_b128 v[228:231], v121 offset:25600
	s_waitcnt lgkmcnt(6)
	v_mfma_f32_16x16x32_bf16 v[64:67], v[232:235], v[40:43], v[64:67]
	v_cvt_pk_bf16_f32 v200, v80, v81
	v_mfma_f32_16x16x32_bf16 v[68:71], v[236:239], v[40:43], v[68:71]
	v_cvt_pk_bf16_f32 v201, v82, v83
	v_mfma_f32_16x16x32_bf16 v[60:63], v[236:239], v[44:47], v[60:63]
	v_cvt_pk_bf16_f32 v202, v76, v77
	v_mfma_f32_16x16x32_bf16 v[56:59], v[232:235], v[44:47], v[56:59]
	v_cvt_pk_bf16_f32 v203, v78, v79
	ds_read_b128 v[232:235], v121 offset:26624
	ds_read_b128 v[236:239], v121 offset:27648
	s_waitcnt lgkmcnt(6)
	ds_read_b128 v[152:155], v183 offset:1024
	ds_read_b128 v[156:159], v183 offset:1088
	v_mfma_f32_16x16x32_bf16 v[64:67], v[240:243], v[48:51], v[64:67]
	v_cvt_pk_bf16_f32 v204, v84, v85
	v_mfma_f32_16x16x32_bf16 v[68:71], v[244:247], v[48:51], v[68:71]
	v_cvt_pk_bf16_f32 v205, v86, v87
	v_mfma_f32_16x16x32_bf16 v[60:63], v[244:247], v[52:55], v[60:63]
	v_cvt_pk_bf16_f32 v206, v72, v73
	v_mfma_f32_16x16x32_bf16 v[56:59], v[240:243], v[52:55], v[56:59]
	v_cvt_pk_bf16_f32 v207, v74, v75
	ds_read_b128 v[240:243], v121 offset:28672
	ds_read_b128 v[244:247], v121 offset:29696
	s_waitcnt lgkmcnt(8)
	v_mfma_f32_16x16x32_bf16 v[64:67], v[248:251], v[112:115], v[64:67]
	v_pk_max_i16 v200, v200, 0
	v_mfma_f32_16x16x32_bf16 v[68:71], v[252:255], v[112:115], v[68:71]
	v_pk_max_i16 v201, v201, 0
	v_mfma_f32_16x16x32_bf16 v[60:63], v[252:255], v[116:119], v[60:63]
	v_pk_max_i16 v202, v202, 0
	v_mfma_f32_16x16x32_bf16 v[56:59], v[248:251], v[116:119], v[56:59]
	v_pk_max_i16 v203, v203, 0
	ds_read_b128 v[248:251], v121 offset:30720
	ds_read_b128 v[252:255], v121 offset:31744
	s_setprio 1
	s_waitcnt lgkmcnt(8)
	v_mfma_f32_16x16x32_bf16 v[80:83], v[224:227], v[0:3], v[160:163]
	v_pk_max_i16 v204, v204, 0
	v_mfma_f32_16x16x32_bf16 v[76:79], v[228:231], v[0:3], v[164:167]
	v_pk_max_i16 v205, v205, 0
	v_mfma_f32_16x16x32_bf16 v[72:75], v[228:231], v[4:7], v[164:167]
	v_pk_max_i16 v206, v206, 0
	v_mfma_f32_16x16x32_bf16 v[84:87], v[224:227], v[4:7], v[160:163]
	v_pk_max_i16 v207, v207, 0
	ds_read_b128 v[224:227], v121 offset:32768
	ds_read_b128 v[228:231], v121 offset:33792
	s_waitcnt lgkmcnt(8)
	v_mfma_f32_16x16x32_bf16 v[80:83], v[232:235], v[12:15], v[80:83]
	v_cvt_pk_bf16_f32 v208, v64, v65
	v_mfma_f32_16x16x32_bf16 v[76:79], v[236:239], v[12:15], v[76:79]
	v_cvt_pk_bf16_f32 v209, v66, v67
	v_mfma_f32_16x16x32_bf16 v[72:75], v[236:239], v[8:11], v[72:75]
	v_cvt_pk_bf16_f32 v210, v68, v69
	v_mfma_f32_16x16x32_bf16 v[84:87], v[232:235], v[8:11], v[84:87]
	v_cvt_pk_bf16_f32 v211, v70, v71
	ds_read_b128 v[232:235], v121 offset:34816
	ds_read_b128 v[236:239], v121 offset:35840
	s_waitcnt lgkmcnt(6)
	v_mfma_f32_16x16x32_bf16 v[80:83], v[240:243], v[16:19], v[80:83]
	v_cvt_pk_bf16_f32 v212, v56, v57
	v_mfma_f32_16x16x32_bf16 v[76:79], v[244:247], v[16:19], v[76:79]
	v_cvt_pk_bf16_f32 v213, v58, v59
	v_mfma_f32_16x16x32_bf16 v[72:75], v[244:247], v[20:23], v[72:75]
	v_cvt_pk_bf16_f32 v214, v60, v61
	v_mfma_f32_16x16x32_bf16 v[84:87], v[240:243], v[20:23], v[84:87]
	v_cvt_pk_bf16_f32 v215, v62, v63
	ds_read_b128 v[240:243], v121 offset:36864
	ds_read_b128 v[244:247], v121 offset:37888
	s_waitcnt lgkmcnt(6)
	v_mfma_f32_16x16x32_bf16 v[80:83], v[248:251], v[24:27], v[80:83]
	v_pk_max_i16 v208, v208, 0
	v_mfma_f32_16x16x32_bf16 v[76:79], v[252:255], v[24:27], v[76:79]
	v_pk_max_i16 v209, v209, 0
	v_mfma_f32_16x16x32_bf16 v[72:75], v[252:255], v[28:31], v[72:75]
	v_pk_max_i16 v210, v210, 0
	v_mfma_f32_16x16x32_bf16 v[84:87], v[248:251], v[28:31], v[84:87]
	v_pk_max_i16 v211, v211, 0
	ds_read_b128 v[248:251], v121 offset:38912
	ds_read_b128 v[252:255], v121 offset:39936
	s_setprio 0
	s_waitcnt lgkmcnt(6)
	v_mfma_f32_16x16x32_bf16 v[80:83], v[224:227], v[32:35], v[80:83]
	v_pk_max_i16 v212, v212, 0
	v_mfma_f32_16x16x32_bf16 v[76:79], v[228:231], v[32:35], v[76:79]
	v_pk_max_i16 v213, v213, 0
	v_mfma_f32_16x16x32_bf16 v[72:75], v[228:231], v[36:39], v[72:75]
	v_pk_max_i16 v214, v214, 0
	v_mfma_f32_16x16x32_bf16 v[84:87], v[224:227], v[36:39], v[84:87]
	v_pk_max_i16 v215, v215, 0
	s_waitcnt lgkmcnt(4)
	v_mfma_f32_16x16x32_bf16 v[80:83], v[232:235], v[40:43], v[80:83]
	v_mfma_f32_16x16x32_bf16 v[76:79], v[236:239], v[40:43], v[76:79]
	v_mfma_f32_16x16x32_bf16 v[72:75], v[236:239], v[44:47], v[72:75]
	v_mfma_f32_16x16x32_bf16 v[84:87], v[232:235], v[44:47], v[84:87]
	s_cmp_eq_u32 s52, 3
	s_cbranch_scc1 .Lnerf_head
.Lnerf_hid_a4:
	s_waitcnt vmcnt(0) lgkmcnt(0)
	s_barrier
	v_mfma_f32_16x16x32_bf16 v[80:83], v[240:243], v[48:51], v[80:83]
	ds_read_b128 v[224:227], v121 offset:40960
	ds_read_b128 v[228:231], v121 offset:41984
	v_mfma_f32_16x16x32_bf16 v[76:79], v[244:247], v[48:51], v[76:79]
	ds_read_b128 v[232:235], v121 offset:43008
	v_mfma_f32_16x16x32_bf16 v[72:75], v[244:247], v[52:55], v[72:75]
	ds_read_b128 v[236:239], v121 offset:44032
	v_mfma_f32_16x16x32_bf16 v[84:87], v[240:243], v[52:55], v[84:87]
	ds_read_b128 v[240:243], v121 offset:45056
	ds_read_b128 v[244:247], v121 offset:46080
	v_mfma_f32_16x16x32_bf16 v[80:83], v[248:251], v[112:115], v[80:83]
	v_mfma_f32_16x16x32_bf16 v[76:79], v[252:255], v[112:115], v[76:79]
	v_mfma_f32_16x16x32_bf16 v[72:75], v[252:255], v[116:119], v[72:75]
	v_mfma_f32_16x16x32_bf16 v[84:87], v[248:251], v[116:119], v[84:87]
	ds_read_b128 v[248:251], v121 offset:47104
	ds_read_b128 v[252:255], v121 offset:48128
	s_setprio 3
	s_waitcnt lgkmcnt(6)
	v_mfma_f32_16x16x32_bf16 v[64:67], v[224:227], v[88:91], v[152:155]
	v_mfma_f32_16x16x32_bf16 v[68:71], v[228:231], v[88:91], v[156:159]
	v_mfma_f32_16x16x32_bf16 v[60:63], v[228:231], v[92:95], v[156:159]
	v_mfma_f32_16x16x32_bf16 v[56:59], v[224:227], v[92:95], v[152:155]
	ds_read_b128 v[224:227], v121 offset:49152
	ds_read_b128 v[228:231], v121 offset:50176
	s_waitcnt lgkmcnt(6)
	ds_read_b128 v[160:163], v183 offset:1152
	ds_read_b128 v[164:167], v183 offset:1216
	v_mfma_f32_16x16x32_bf16 v[64:67], v[232:235], v[96:99], v[64:67]
	v_mfma_f32_16x16x32_bf16 v[68:71], v[236:239], v[96:99], v[68:71]
	s_mov_b32 m0, s35
	s_add_i32 s51, s50, 0x20000
	v_mfma_f32_16x16x32_bf16 v[60:63], v[236:239], v[100:103], v[60:63]
	buffer_load_dwordx4 v125, s[36:39], s51 offen lds
	v_mfma_f32_16x16x32_bf16 v[56:59], v[232:235], v[100:103], v[56:59]
	ds_read_b128 v[232:235], v121 offset:51200
	ds_read_b128 v[236:239], v121 offset:52224
	s_waitcnt lgkmcnt(8)
	v_mfma_f32_16x16x32_bf16 v[64:67], v[240:243], v[104:107], v[64:67]
	v_mfma_f32_16x16x32_bf16 v[68:71], v[244:247], v[104:107], v[68:71]
	s_mov_b32 m0, s42
	s_add_i32 s51, s50, 0x22000
	v_mfma_f32_16x16x32_bf16 v[60:63], v[244:247], v[108:111], v[60:63]
	buffer_load_dwordx4 v125, s[36:39], s51 offen lds
	v_mfma_f32_16x16x32_bf16 v[56:59], v[240:243], v[108:111], v[56:59]
	ds_read_b128 v[240:243], v121 offset:53248
	ds_read_b128 v[244:247], v121 offset:54272
	s_waitcnt lgkmcnt(8)
	v_mfma_f32_16x16x32_bf16 v[64:67], v[248:251], v[184:187], v[64:67]
	v_cvt_pk_bf16_f32 v216, v80, v81
	v_mfma_f32_16x16x32_bf16 v[68:71], v[252:255], v[184:187], v[68:71]
	s_mov_b32 m0, s41
	s_add_i32 s51, s50, 0x24000
	v_cvt_pk_bf16_f32 v217, v82, v83
	v_mfma_f32_16x16x32_bf16 v[60:63], v[252:255], v[188:191], v[60:63]
	buffer_load_dwordx4 v125, s[36:39], s51 offen lds
	v_cvt_pk_bf16_f32 v218, v76, v77
	v_mfma_f32_16x16x32_bf16 v[56:59], v[248:251], v[188:191], v[56:59]
	v_cvt_pk_bf16_f32 v219, v78, v79
	ds_read_b128 v[248:251], v121 offset:55296
	ds_read_b128 v[252:255], v121 offset:56320
	s_setprio 2
	s_waitcnt lgkmcnt(8)
	v_mfma_f32_16x16x32_bf16 v[64:67], v[224:227], v[192:195], v[64:67]
	v_cvt_pk_bf16_f32 v220, v84, v85
	v_mfma_f32_16x16x32_bf16 v[68:71], v[228:231], v[192:195], v[68:71]
	s_mov_b32 m0, s40
	s_add_i32 s51, s50, 0x26000
	v_cvt_pk_bf16_f32 v221, v86, v87
	v_mfma_f32_16x16x32_bf16 v[60:63], v[228:231], v[196:199], v[60:63]
	buffer_load_dwordx4 v125, s[36:39], s51 offen lds
	v_cvt_pk_bf16_f32 v222, v72, v73
	v_mfma_f32_16x16x32_bf16 v[56:59], v[224:227], v[196:199], v[56:59]
	v_cvt_pk_bf16_f32 v223, v74, v75
	ds_read_b128 v[224:227], v121 offset:57344
	ds_read_b128 v[228:231], v121 offset:58368
	s_waitcnt lgkmcnt(6)
	v_mfma_f32_16x16x32_bf16 v[64:67], v[232:235], v[200:203], v[64:67]
	v_pk_max_i16 v216, v216, 0
	v_mfma_f32_16x16x32_bf16 v[68:71], v[236:239], v[200:203], v[68:71]
	v_pk_max_i16 v217, v217, 0
	v_mfma_f32_16x16x32_bf16 v[60:63], v[236:239], v[204:207], v[60:63]
	v_pk_max_i16 v218, v218, 0
	v_mfma_f32_16x16x32_bf16 v[56:59], v[232:235], v[204:207], v[56:59]
	v_pk_max_i16 v219, v219, 0
	ds_read_b128 v[232:235], v121 offset:59392
	ds_read_b128 v[236:239], v121 offset:60416
	s_waitcnt lgkmcnt(6)
	ds_read_b128 v[152:155], v183 offset:1280
	ds_read_b128 v[156:159], v183 offset:1344
	v_mfma_f32_16x16x32_bf16 v[64:67], v[240:243], v[208:211], v[64:67]
	v_pk_max_i16 v220, v220, 0
	v_mfma_f32_16x16x32_bf16 v[68:71], v[244:247], v[208:211], v[68:71]
	v_pk_max_i16 v221, v221, 0
	v_mfma_f32_16x16x32_bf16 v[60:63], v[244:247], v[212:215], v[60:63]
	v_pk_max_i16 v222, v222, 0
	v_mfma_f32_16x16x32_bf16 v[56:59], v[240:243], v[212:215], v[56:59]
	v_pk_max_i16 v223, v223, 0
	ds_read_b128 v[240:243], v121 offset:61440
	ds_read_b128 v[244:247], v121 offset:62464
	s_waitcnt lgkmcnt(8)
	v_mfma_f32_16x16x32_bf16 v[64:67], v[248:251], v[216:219], v[64:67]
	v_mfma_f32_16x16x32_bf16 v[68:71], v[252:255], v[216:219], v[68:71]
	v_mfma_f32_16x16x32_bf16 v[60:63], v[252:255], v[220:223], v[60:63]
	v_mfma_f32_16x16x32_bf16 v[56:59], v[248:251], v[220:223], v[56:59]
	ds_read_b128 v[248:251], v121 offset:63488
	ds_read_b128 v[252:255], v121 offset:64512
	s_setprio 1
	s_waitcnt lgkmcnt(8)
	v_mfma_f32_16x16x32_bf16 v[80:83], v[224:227], v[88:91], v[160:163]
	v_mfma_f32_16x16x32_bf16 v[76:79], v[228:231], v[88:91], v[164:167]
	v_mfma_f32_16x16x32_bf16 v[72:75], v[228:231], v[92:95], v[164:167]
	v_mfma_f32_16x16x32_bf16 v[84:87], v[224:227], v[92:95], v[160:163]
	ds_read_b128 v[224:227], v126 offset:57344
	ds_read_b128 v[228:231], v126 offset:58368
	s_waitcnt lgkmcnt(8)
	v_mfma_f32_16x16x32_bf16 v[80:83], v[232:235], v[96:99], v[80:83]
	v_cvt_pk_bf16_f32 v0, v64, v65
	v_mfma_f32_16x16x32_bf16 v[76:79], v[236:239], v[96:99], v[76:79]
	v_cvt_pk_bf16_f32 v1, v66, v67
	v_mfma_f32_16x16x32_bf16 v[72:75], v[236:239], v[100:103], v[72:75]
	v_cvt_pk_bf16_f32 v2, v68, v69
	v_mfma_f32_16x16x32_bf16 v[84:87], v[232:235], v[100:103], v[84:87]
	v_cvt_pk_bf16_f32 v3, v70, v71
	ds_read_b128 v[232:235], v126 offset:59392
	ds_read_b128 v[236:239], v126 offset:60416
	s_waitcnt lgkmcnt(6)
	v_mfma_f32_16x16x32_bf16 v[80:83], v[240:243], v[104:107], v[80:83]
	v_cvt_pk_bf16_f32 v4, v56, v57
	v_mfma_f32_16x16x32_bf16 v[76:79], v[244:247], v[104:107], v[76:79]
	v_cvt_pk_bf16_f32 v5, v58, v59
	v_mfma_f32_16x16x32_bf16 v[72:75], v[244:247], v[108:111], v[72:75]
	v_cvt_pk_bf16_f32 v6, v60, v61
	v_mfma_f32_16x16x32_bf16 v[84:87], v[240:243], v[108:111], v[84:87]
	v_cvt_pk_bf16_f32 v7, v62, v63
	ds_read_b128 v[240:243], v126 offset:61440
	ds_read_b128 v[244:247], v126 offset:62464
	s_waitcnt lgkmcnt(6)
	v_mfma_f32_16x16x32_bf16 v[80:83], v[248:251], v[184:187], v[80:83]
	v_pk_max_i16 v0, v0, 0
	v_mfma_f32_16x16x32_bf16 v[76:79], v[252:255], v[184:187], v[76:79]
	v_pk_max_i16 v1, v1, 0
	v_mfma_f32_16x16x32_bf16 v[72:75], v[252:255], v[188:191], v[72:75]
	v_pk_max_i16 v2, v2, 0
	v_mfma_f32_16x16x32_bf16 v[84:87], v[248:251], v[188:191], v[84:87]
	v_pk_max_i16 v3, v3, 0
	ds_read_b128 v[248:251], v126 offset:63488
	ds_read_b128 v[252:255], v126 offset:64512
	s_setprio 0
	s_waitcnt lgkmcnt(6)
	v_mfma_f32_16x16x32_bf16 v[80:83], v[224:227], v[192:195], v[80:83]
	v_pk_max_i16 v4, v4, 0
	v_mfma_f32_16x16x32_bf16 v[76:79], v[228:231], v[192:195], v[76:79]
	v_pk_max_i16 v5, v5, 0
	v_mfma_f32_16x16x32_bf16 v[72:75], v[228:231], v[196:199], v[72:75]
	v_pk_max_i16 v6, v6, 0
	v_mfma_f32_16x16x32_bf16 v[84:87], v[224:227], v[196:199], v[84:87]
	v_pk_max_i16 v7, v7, 0
	s_waitcnt lgkmcnt(4)
	v_mfma_f32_16x16x32_bf16 v[80:83], v[232:235], v[200:203], v[80:83]
	v_mfma_f32_16x16x32_bf16 v[76:79], v[236:239], v[200:203], v[76:79]
	v_mfma_f32_16x16x32_bf16 v[72:75], v[236:239], v[204:207], v[72:75]
	v_mfma_f32_16x16x32_bf16 v[84:87], v[232:235], v[204:207], v[84:87]
.Lnerf_hid_a5:
	s_waitcnt vmcnt(0) lgkmcnt(0)
	s_barrier
	v_mfma_f32_16x16x32_bf16 v[80:83], v[240:243], v[208:211], v[80:83]
	ds_read_b128 v[224:227], v121 offset:8192
	ds_read_b128 v[228:231], v121 offset:9216
	v_mfma_f32_16x16x32_bf16 v[76:79], v[244:247], v[208:211], v[76:79]
	ds_read_b128 v[232:235], v121 offset:10240
	v_mfma_f32_16x16x32_bf16 v[72:75], v[244:247], v[212:215], v[72:75]
	ds_read_b128 v[236:239], v121 offset:11264
	v_mfma_f32_16x16x32_bf16 v[84:87], v[240:243], v[212:215], v[84:87]
	ds_read_b128 v[240:243], v121 offset:12288
	ds_read_b128 v[244:247], v121 offset:13312
	v_mfma_f32_16x16x32_bf16 v[80:83], v[248:251], v[216:219], v[80:83]
	v_mfma_f32_16x16x32_bf16 v[76:79], v[252:255], v[216:219], v[76:79]
	v_mfma_f32_16x16x32_bf16 v[72:75], v[252:255], v[220:223], v[72:75]
	v_mfma_f32_16x16x32_bf16 v[84:87], v[248:251], v[220:223], v[84:87]
	ds_read_b128 v[248:251], v121 offset:14336
	ds_read_b128 v[252:255], v121 offset:15360
	s_setprio 3
	s_waitcnt lgkmcnt(6)
	v_mfma_f32_16x16x32_bf16 v[64:67], v[224:227], v[88:91], v[152:155]
	v_mfma_f32_16x16x32_bf16 v[68:71], v[228:231], v[88:91], v[156:159]
	v_mfma_f32_16x16x32_bf16 v[60:63], v[228:231], v[92:95], v[156:159]
	v_mfma_f32_16x16x32_bf16 v[56:59], v[224:227], v[92:95], v[152:155]
	ds_read_b128 v[224:227], v121 offset:16384
	ds_read_b128 v[228:231], v121 offset:17408
	s_waitcnt lgkmcnt(6)
	ds_read_b128 v[160:163], v183 offset:1408
	ds_read_b128 v[164:167], v183 offset:1472
	v_mfma_f32_16x16x32_bf16 v[64:67], v[232:235], v[96:99], v[64:67]
	v_mfma_f32_16x16x32_bf16 v[68:71], v[236:239], v[96:99], v[68:71]
	s_mov_b32 m0, s28
	s_add_i32 s51, s50, 0x28000
	v_mfma_f32_16x16x32_bf16 v[60:63], v[236:239], v[100:103], v[60:63]
	buffer_load_dwordx4 v125, s[36:39], s51 offen lds
	v_mfma_f32_16x16x32_bf16 v[56:59], v[232:235], v[100:103], v[56:59]
	ds_read_b128 v[232:235], v121 offset:18432
	ds_read_b128 v[236:239], v121 offset:19456
	s_waitcnt lgkmcnt(8)
	v_mfma_f32_16x16x32_bf16 v[64:67], v[240:243], v[104:107], v[64:67]
	v_mfma_f32_16x16x32_bf16 v[68:71], v[244:247], v[104:107], v[68:71]
	s_mov_b32 m0, s29
	s_add_i32 s51, s50, 0x2a000
	v_mfma_f32_16x16x32_bf16 v[60:63], v[244:247], v[108:111], v[60:63]
	buffer_load_dwordx4 v125, s[36:39], s51 offen lds
	v_mfma_f32_16x16x32_bf16 v[56:59], v[240:243], v[108:111], v[56:59]
	ds_read_b128 v[240:243], v121 offset:20480
	ds_read_b128 v[244:247], v121 offset:21504
	s_waitcnt lgkmcnt(8)
	v_mfma_f32_16x16x32_bf16 v[64:67], v[248:251], v[184:187], v[64:67]
	v_mfma_f32_16x16x32_bf16 v[68:71], v[252:255], v[184:187], v[68:71]
	s_mov_b32 m0, s33
	s_add_i32 s51, s50, 0x2c000
	v_mfma_f32_16x16x32_bf16 v[60:63], v[252:255], v[188:191], v[60:63]
	buffer_load_dwordx4 v125, s[36:39], s51 offen lds
	v_mfma_f32_16x16x32_bf16 v[56:59], v[248:251], v[188:191], v[56:59]
	ds_read_b128 v[248:251], v121 offset:22528
	ds_read_b128 v[252:255], v121 offset:23552
	s_setprio 2
	s_waitcnt lgkmcnt(8)
	v_mfma_f32_16x16x32_bf16 v[64:67], v[224:227], v[192:195], v[64:67]
	v_mfma_f32_16x16x32_bf16 v[68:71], v[228:231], v[192:195], v[68:71]
	s_mov_b32 m0, s34
	s_add_i32 s51, s50, 0x2e000
	v_mfma_f32_16x16x32_bf16 v[60:63], v[228:231], v[196:199], v[60:63]
	buffer_load_dwordx4 v125, s[36:39], s51 offen lds
	v_mfma_f32_16x16x32_bf16 v[56:59], v[224:227], v[196:199], v[56:59]
	ds_read_b128 v[224:227], v121 offset:24576
	ds_read_b128 v[228:231], v121 offset:25600
	s_waitcnt lgkmcnt(6)
	v_mfma_f32_16x16x32_bf16 v[64:67], v[232:235], v[200:203], v[64:67]
	v_cvt_pk_bf16_f32 v12, v80, v81
	v_mfma_f32_16x16x32_bf16 v[68:71], v[236:239], v[200:203], v[68:71]
	v_cvt_pk_bf16_f32 v13, v82, v83
	v_mfma_f32_16x16x32_bf16 v[60:63], v[236:239], v[204:207], v[60:63]
	v_cvt_pk_bf16_f32 v14, v76, v77
	v_mfma_f32_16x16x32_bf16 v[56:59], v[232:235], v[204:207], v[56:59]
	v_cvt_pk_bf16_f32 v15, v78, v79
	ds_read_b128 v[232:235], v121 offset:26624
	ds_read_b128 v[236:239], v121 offset:27648
	s_waitcnt lgkmcnt(6)
	ds_read_b128 v[152:155], v183 offset:1536
	ds_read_b128 v[156:159], v183 offset:1600
	v_mfma_f32_16x16x32_bf16 v[64:67], v[240:243], v[208:211], v[64:67]
	v_cvt_pk_bf16_f32 v8, v84, v85
	v_mfma_f32_16x16x32_bf16 v[68:71], v[244:247], v[208:211], v[68:71]
	v_cvt_pk_bf16_f32 v9, v86, v87
	v_mfma_f32_16x16x32_bf16 v[60:63], v[244:247], v[212:215], v[60:63]
	v_cvt_pk_bf16_f32 v10, v72, v73
	v_mfma_f32_16x16x32_bf16 v[56:59], v[240:243], v[212:215], v[56:59]
	v_cvt_pk_bf16_f32 v11, v74, v75
	ds_read_b128 v[240:243], v121 offset:28672
	ds_read_b128 v[244:247], v121 offset:29696
	s_waitcnt lgkmcnt(8)
	v_mfma_f32_16x16x32_bf16 v[64:67], v[248:251], v[216:219], v[64:67]
	v_pk_max_i16 v12, v12, 0
	v_mfma_f32_16x16x32_bf16 v[68:71], v[252:255], v[216:219], v[68:71]
	v_pk_max_i16 v13, v13, 0
	v_mfma_f32_16x16x32_bf16 v[60:63], v[252:255], v[220:223], v[60:63]
	v_pk_max_i16 v14, v14, 0
	v_mfma_f32_16x16x32_bf16 v[56:59], v[248:251], v[220:223], v[56:59]
	v_pk_max_i16 v15, v15, 0
	ds_read_b128 v[248:251], v121 offset:30720
	ds_read_b128 v[252:255], v121 offset:31744
	s_setprio 1
	s_waitcnt lgkmcnt(8)
	v_mfma_f32_16x16x32_bf16 v[80:83], v[224:227], v[88:91], v[160:163]
	v_pk_max_i16 v8, v8, 0
	v_mfma_f32_16x16x32_bf16 v[76:79], v[228:231], v[88:91], v[164:167]
	v_pk_max_i16 v9, v9, 0
	v_mfma_f32_16x16x32_bf16 v[72:75], v[228:231], v[92:95], v[164:167]
	v_pk_max_i16 v10, v10, 0
	v_mfma_f32_16x16x32_bf16 v[84:87], v[224:227], v[92:95], v[160:163]
	v_pk_max_i16 v11, v11, 0
	ds_read_b128 v[224:227], v121 offset:32768
	ds_read_b128 v[228:231], v121 offset:33792
	s_waitcnt lgkmcnt(8)
	v_mfma_f32_16x16x32_bf16 v[80:83], v[232:235], v[96:99], v[80:83]
	v_cvt_pk_bf16_f32 v16, v64, v65
	v_mfma_f32_16x16x32_bf16 v[76:79], v[236:239], v[96:99], v[76:79]
	v_cvt_pk_bf16_f32 v17, v66, v67
	v_mfma_f32_16x16x32_bf16 v[72:75], v[236:239], v[100:103], v[72:75]
	v_cvt_pk_bf16_f32 v18, v68, v69
	v_mfma_f32_16x16x32_bf16 v[84:87], v[232:235], v[100:103], v[84:87]
	v_cvt_pk_bf16_f32 v19, v70, v71
	ds_read_b128 v[232:235], v121 offset:34816
	ds_read_b128 v[236:239], v121 offset:35840
	s_waitcnt lgkmcnt(6)
	v_mfma_f32_16x16x32_bf16 v[80:83], v[240:243], v[104:107], v[80:83]
	v_cvt_pk_bf16_f32 v20, v56, v57
	v_mfma_f32_16x16x32_bf16 v[76:79], v[244:247], v[104:107], v[76:79]
	v_cvt_pk_bf16_f32 v21, v58, v59
	v_mfma_f32_16x16x32_bf16 v[72:75], v[244:247], v[108:111], v[72:75]
	v_cvt_pk_bf16_f32 v22, v60, v61
	v_mfma_f32_16x16x32_bf16 v[84:87], v[240:243], v[108:111], v[84:87]
	v_cvt_pk_bf16_f32 v23, v62, v63
	ds_read_b128 v[240:243], v121 offset:36864
	ds_read_b128 v[244:247], v121 offset:37888
	s_waitcnt lgkmcnt(6)
	v_mfma_f32_16x16x32_bf16 v[80:83], v[248:251], v[184:187], v[80:83]
	v_pk_max_i16 v16, v16, 0
	v_mfma_f32_16x16x32_bf16 v[76:79], v[252:255], v[184:187], v[76:79]
	v_pk_max_i16 v17, v17, 0
	v_mfma_f32_16x16x32_bf16 v[72:75], v[252:255], v[188:191], v[72:75]
	v_pk_max_i16 v18, v18, 0
	v_mfma_f32_16x16x32_bf16 v[84:87], v[248:251], v[188:191], v[84:87]
	v_pk_max_i16 v19, v19, 0
	ds_read_b128 v[248:251], v121 offset:38912
	ds_read_b128 v[252:255], v121 offset:39936
	s_setprio 0
	s_waitcnt lgkmcnt(6)
	v_mfma_f32_16x16x32_bf16 v[80:83], v[224:227], v[192:195], v[80:83]
	v_pk_max_i16 v20, v20, 0
	v_mfma_f32_16x16x32_bf16 v[76:79], v[228:231], v[192:195], v[76:79]
	v_pk_max_i16 v21, v21, 0
	v_mfma_f32_16x16x32_bf16 v[72:75], v[228:231], v[196:199], v[72:75]
	v_pk_max_i16 v22, v22, 0
	v_mfma_f32_16x16x32_bf16 v[84:87], v[224:227], v[196:199], v[84:87]
	v_pk_max_i16 v23, v23, 0
	s_waitcnt lgkmcnt(4)
	v_mfma_f32_16x16x32_bf16 v[80:83], v[232:235], v[200:203], v[80:83]
	v_mfma_f32_16x16x32_bf16 v[76:79], v[236:239], v[200:203], v[76:79]
	v_mfma_f32_16x16x32_bf16 v[72:75], v[236:239], v[204:207], v[72:75]
	v_mfma_f32_16x16x32_bf16 v[84:87], v[232:235], v[204:207], v[84:87]
.Lnerf_hid_a6:
	s_waitcnt vmcnt(0) lgkmcnt(0)
	s_barrier
	v_mfma_f32_16x16x32_bf16 v[80:83], v[240:243], v[208:211], v[80:83]
	ds_read_b128 v[224:227], v121 offset:40960
	ds_read_b128 v[228:231], v121 offset:41984
	v_mfma_f32_16x16x32_bf16 v[76:79], v[244:247], v[208:211], v[76:79]
	ds_read_b128 v[232:235], v121 offset:43008
	v_mfma_f32_16x16x32_bf16 v[72:75], v[244:247], v[212:215], v[72:75]
	ds_read_b128 v[236:239], v121 offset:44032
	v_mfma_f32_16x16x32_bf16 v[84:87], v[240:243], v[212:215], v[84:87]
	ds_read_b128 v[240:243], v121 offset:45056
	ds_read_b128 v[244:247], v121 offset:46080
	v_mfma_f32_16x16x32_bf16 v[80:83], v[248:251], v[216:219], v[80:83]
	v_mfma_f32_16x16x32_bf16 v[76:79], v[252:255], v[216:219], v[76:79]
	v_mfma_f32_16x16x32_bf16 v[72:75], v[252:255], v[220:223], v[72:75]
	v_mfma_f32_16x16x32_bf16 v[84:87], v[248:251], v[220:223], v[84:87]
	ds_read_b128 v[248:251], v121 offset:47104
	ds_read_b128 v[252:255], v121 offset:48128
	s_setprio 3
	s_waitcnt lgkmcnt(6)
	v_mfma_f32_16x16x32_bf16 v[64:67], v[224:227], v[88:91], v[152:155]
	v_mfma_f32_16x16x32_bf16 v[68:71], v[228:231], v[88:91], v[156:159]
	v_mfma_f32_16x16x32_bf16 v[60:63], v[228:231], v[92:95], v[156:159]
	v_mfma_f32_16x16x32_bf16 v[56:59], v[224:227], v[92:95], v[152:155]
	ds_read_b128 v[224:227], v121 offset:49152
	ds_read_b128 v[228:231], v121 offset:50176
	s_waitcnt lgkmcnt(6)
	ds_read_b128 v[160:163], v183 offset:1664
	ds_read_b128 v[164:167], v183 offset:1728
	v_mfma_f32_16x16x32_bf16 v[64:67], v[232:235], v[96:99], v[64:67]
	v_mfma_f32_16x16x32_bf16 v[68:71], v[236:239], v[96:99], v[68:71]
	s_mov_b32 m0, s35
	s_add_i32 s51, s50, 0x30000
	v_mfma_f32_16x16x32_bf16 v[60:63], v[236:239], v[100:103], v[60:63]
	buffer_load_dwordx4 v125, s[36:39], s51 offen lds
	v_mfma_f32_16x16x32_bf16 v[56:59], v[232:235], v[100:103], v[56:59]
	ds_read_b128 v[232:235], v121 offset:51200
	ds_read_b128 v[236:239], v121 offset:52224
	s_waitcnt lgkmcnt(8)
	v_mfma_f32_16x16x32_bf16 v[64:67], v[240:243], v[104:107], v[64:67]
	v_mfma_f32_16x16x32_bf16 v[68:71], v[244:247], v[104:107], v[68:71]
	s_mov_b32 m0, s42
	s_add_i32 s51, s50, 0x32000
	v_mfma_f32_16x16x32_bf16 v[60:63], v[244:247], v[108:111], v[60:63]
	buffer_load_dwordx4 v125, s[36:39], s51 offen lds
	v_mfma_f32_16x16x32_bf16 v[56:59], v[240:243], v[108:111], v[56:59]
	ds_read_b128 v[240:243], v121 offset:53248
	ds_read_b128 v[244:247], v121 offset:54272
	s_waitcnt lgkmcnt(8)
	v_mfma_f32_16x16x32_bf16 v[64:67], v[248:251], v[184:187], v[64:67]
	v_mfma_f32_16x16x32_bf16 v[68:71], v[252:255], v[184:187], v[68:71]
	s_mov_b32 m0, s41
	s_add_i32 s51, s50, 0x34000
	v_mfma_f32_16x16x32_bf16 v[60:63], v[252:255], v[188:191], v[60:63]
	buffer_load_dwordx4 v125, s[36:39], s51 offen lds
	v_mfma_f32_16x16x32_bf16 v[56:59], v[248:251], v[188:191], v[56:59]
	ds_read_b128 v[248:251], v121 offset:55296
	ds_read_b128 v[252:255], v121 offset:56320
	s_setprio 2
	s_waitcnt lgkmcnt(8)
	v_mfma_f32_16x16x32_bf16 v[64:67], v[224:227], v[192:195], v[64:67]
	v_mfma_f32_16x16x32_bf16 v[68:71], v[228:231], v[192:195], v[68:71]
	s_mov_b32 m0, s40
	s_add_i32 s51, s50, 0x36000
	v_mfma_f32_16x16x32_bf16 v[60:63], v[228:231], v[196:199], v[60:63]
	buffer_load_dwordx4 v125, s[36:39], s51 offen lds
	v_mfma_f32_16x16x32_bf16 v[56:59], v[224:227], v[196:199], v[56:59]
	ds_read_b128 v[224:227], v121 offset:57344
	ds_read_b128 v[228:231], v121 offset:58368
	s_waitcnt lgkmcnt(6)
	v_mfma_f32_16x16x32_bf16 v[64:67], v[232:235], v[200:203], v[64:67]
	v_cvt_pk_bf16_f32 v24, v80, v81
	v_mfma_f32_16x16x32_bf16 v[68:71], v[236:239], v[200:203], v[68:71]
	v_cvt_pk_bf16_f32 v25, v82, v83
	v_mfma_f32_16x16x32_bf16 v[60:63], v[236:239], v[204:207], v[60:63]
	v_cvt_pk_bf16_f32 v26, v76, v77
	v_mfma_f32_16x16x32_bf16 v[56:59], v[232:235], v[204:207], v[56:59]
	v_cvt_pk_bf16_f32 v27, v78, v79
	ds_read_b128 v[232:235], v121 offset:59392
	ds_read_b128 v[236:239], v121 offset:60416
	s_waitcnt lgkmcnt(6)
	ds_read_b128 v[152:155], v183 offset:1792
	ds_read_b128 v[156:159], v183 offset:1856
	v_mfma_f32_16x16x32_bf16 v[64:67], v[240:243], v[208:211], v[64:67]
	v_cvt_pk_bf16_f32 v28, v84, v85
	v_mfma_f32_16x16x32_bf16 v[68:71], v[244:247], v[208:211], v[68:71]
	v_cvt_pk_bf16_f32 v29, v86, v87
	v_mfma_f32_16x16x32_bf16 v[60:63], v[244:247], v[212:215], v[60:63]
	v_cvt_pk_bf16_f32 v30, v72, v73
	v_mfma_f32_16x16x32_bf16 v[56:59], v[240:243], v[212:215], v[56:59]
	v_cvt_pk_bf16_f32 v31, v74, v75
	ds_read_b128 v[240:243], v121 offset:61440
	ds_read_b128 v[244:247], v121 offset:62464
	s_waitcnt lgkmcnt(8)
	v_mfma_f32_16x16x32_bf16 v[64:67], v[248:251], v[216:219], v[64:67]
	v_pk_max_i16 v24, v24, 0
	v_mfma_f32_16x16x32_bf16 v[68:71], v[252:255], v[216:219], v[68:71]
	v_pk_max_i16 v25, v25, 0
	v_mfma_f32_16x16x32_bf16 v[60:63], v[252:255], v[220:223], v[60:63]
	v_pk_max_i16 v26, v26, 0
	v_mfma_f32_16x16x32_bf16 v[56:59], v[248:251], v[220:223], v[56:59]
	v_pk_max_i16 v27, v27, 0
	ds_read_b128 v[248:251], v121 offset:63488
	ds_read_b128 v[252:255], v121 offset:64512
	s_setprio 1
	s_waitcnt lgkmcnt(8)
	v_mfma_f32_16x16x32_bf16 v[80:83], v[224:227], v[88:91], v[160:163]
	v_pk_max_i16 v28, v28, 0
	v_mfma_f32_16x16x32_bf16 v[76:79], v[228:231], v[88:91], v[164:167]
	v_pk_max_i16 v29, v29, 0
	v_mfma_f32_16x16x32_bf16 v[72:75], v[228:231], v[92:95], v[164:167]
	v_pk_max_i16 v30, v30, 0
	v_mfma_f32_16x16x32_bf16 v[84:87], v[224:227], v[92:95], v[160:163]
	v_pk_max_i16 v31, v31, 0
	ds_read_b128 v[224:227], v126 offset:57344
	ds_read_b128 v[228:231], v126 offset:58368
	s_waitcnt lgkmcnt(8)
	v_mfma_f32_16x16x32_bf16 v[80:83], v[232:235], v[96:99], v[80:83]
	v_cvt_pk_bf16_f32 v32, v64, v65
	v_mfma_f32_16x16x32_bf16 v[76:79], v[236:239], v[96:99], v[76:79]
	v_cvt_pk_bf16_f32 v33, v66, v67
	v_mfma_f32_16x16x32_bf16 v[72:75], v[236:239], v[100:103], v[72:75]
	v_cvt_pk_bf16_f32 v34, v68, v69
	v_mfma_f32_16x16x32_bf16 v[84:87], v[232:235], v[100:103], v[84:87]
	v_cvt_pk_bf16_f32 v35, v70, v71
	ds_read_b128 v[232:235], v126 offset:59392
	ds_read_b128 v[236:239], v126 offset:60416
	s_waitcnt lgkmcnt(6)
	v_mfma_f32_16x16x32_bf16 v[80:83], v[240:243], v[104:107], v[80:83]
	v_cvt_pk_bf16_f32 v36, v56, v57
	v_mfma_f32_16x16x32_bf16 v[76:79], v[244:247], v[104:107], v[76:79]
	v_cvt_pk_bf16_f32 v37, v58, v59
	v_mfma_f32_16x16x32_bf16 v[72:75], v[244:247], v[108:111], v[72:75]
	v_cvt_pk_bf16_f32 v38, v60, v61
	v_mfma_f32_16x16x32_bf16 v[84:87], v[240:243], v[108:111], v[84:87]
	v_cvt_pk_bf16_f32 v39, v62, v63
	ds_read_b128 v[240:243], v126 offset:61440
	ds_read_b128 v[244:247], v126 offset:62464
	s_waitcnt lgkmcnt(6)
	v_mfma_f32_16x16x32_bf16 v[80:83], v[248:251], v[184:187], v[80:83]
	v_pk_max_i16 v32, v32, 0
	v_mfma_f32_16x16x32_bf16 v[76:79], v[252:255], v[184:187], v[76:79]
	v_pk_max_i16 v33, v33, 0
	v_mfma_f32_16x16x32_bf16 v[72:75], v[252:255], v[188:191], v[72:75]
	v_pk_max_i16 v34, v34, 0
	v_mfma_f32_16x16x32_bf16 v[84:87], v[248:251], v[188:191], v[84:87]
	v_pk_max_i16 v35, v35, 0
	ds_read_b128 v[248:251], v126 offset:63488
	ds_read_b128 v[252:255], v126 offset:64512
	s_setprio 0
	s_waitcnt lgkmcnt(6)
	v_mfma_f32_16x16x32_bf16 v[80:83], v[224:227], v[192:195], v[80:83]
	v_pk_max_i16 v36, v36, 0
	v_mfma_f32_16x16x32_bf16 v[76:79], v[228:231], v[192:195], v[76:79]
	v_pk_max_i16 v37, v37, 0
	v_mfma_f32_16x16x32_bf16 v[72:75], v[228:231], v[196:199], v[72:75]
	v_pk_max_i16 v38, v38, 0
	v_mfma_f32_16x16x32_bf16 v[84:87], v[224:227], v[196:199], v[84:87]
	v_pk_max_i16 v39, v39, 0
	s_waitcnt lgkmcnt(4)
	v_mfma_f32_16x16x32_bf16 v[80:83], v[232:235], v[200:203], v[80:83]
	v_mfma_f32_16x16x32_bf16 v[76:79], v[236:239], v[200:203], v[76:79]
	v_mfma_f32_16x16x32_bf16 v[72:75], v[236:239], v[204:207], v[72:75]
	v_mfma_f32_16x16x32_bf16 v[84:87], v[232:235], v[204:207], v[84:87]
.Lnerf_hid_a7:
	s_waitcnt vmcnt(0) lgkmcnt(0)
	s_barrier
	v_mfma_f32_16x16x32_bf16 v[80:83], v[240:243], v[208:211], v[80:83]
	ds_read_b128 v[224:227], v121 offset:8192
	ds_read_b128 v[228:231], v121 offset:9216
	v_mfma_f32_16x16x32_bf16 v[76:79], v[244:247], v[208:211], v[76:79]
	ds_read_b128 v[232:235], v121 offset:10240
	v_mfma_f32_16x16x32_bf16 v[72:75], v[244:247], v[212:215], v[72:75]
	ds_read_b128 v[236:239], v121 offset:11264
	v_mfma_f32_16x16x32_bf16 v[84:87], v[240:243], v[212:215], v[84:87]
	ds_read_b128 v[240:243], v121 offset:12288
	ds_read_b128 v[244:247], v121 offset:13312
	v_mfma_f32_16x16x32_bf16 v[80:83], v[248:251], v[216:219], v[80:83]
	v_mfma_f32_16x16x32_bf16 v[76:79], v[252:255], v[216:219], v[76:79]
	v_mfma_f32_16x16x32_bf16 v[72:75], v[252:255], v[220:223], v[72:75]
	v_mfma_f32_16x16x32_bf16 v[84:87], v[248:251], v[220:223], v[84:87]
	ds_read_b128 v[248:251], v121 offset:14336
	ds_read_b128 v[252:255], v121 offset:15360
	s_setprio 3
	s_waitcnt lgkmcnt(6)
	v_mfma_f32_16x16x32_bf16 v[64:67], v[224:227], v[88:91], v[152:155]
	v_mfma_f32_16x16x32_bf16 v[68:71], v[228:231], v[88:91], v[156:159]
	v_mfma_f32_16x16x32_bf16 v[60:63], v[228:231], v[92:95], v[156:159]
	v_mfma_f32_16x16x32_bf16 v[56:59], v[224:227], v[92:95], v[152:155]
	ds_read_b128 v[224:227], v121 offset:16384
	ds_read_b128 v[228:231], v121 offset:17408
	s_waitcnt lgkmcnt(6)
	ds_read_b128 v[160:163], v183 offset:1920
	ds_read_b128 v[164:167], v183 offset:1984
	v_mfma_f32_16x16x32_bf16 v[64:67], v[232:235], v[96:99], v[64:67]
	v_mfma_f32_16x16x32_bf16 v[68:71], v[236:239], v[96:99], v[68:71]
	s_mov_b32 m0, s28
	s_add_i32 s51, s50, 0x38000
	v_mfma_f32_16x16x32_bf16 v[60:63], v[236:239], v[100:103], v[60:63]
	buffer_load_dwordx4 v125, s[36:39], s51 offen lds
	v_mfma_f32_16x16x32_bf16 v[56:59], v[232:235], v[100:103], v[56:59]
	ds_read_b128 v[232:235], v121 offset:18432
	ds_read_b128 v[236:239], v121 offset:19456
	s_waitcnt lgkmcnt(8)
	v_mfma_f32_16x16x32_bf16 v[64:67], v[240:243], v[104:107], v[64:67]
	v_mfma_f32_16x16x32_bf16 v[68:71], v[244:247], v[104:107], v[68:71]
	s_mov_b32 m0, s29
	s_add_i32 s51, s50, 0x3a000
	v_mfma_f32_16x16x32_bf16 v[60:63], v[244:247], v[108:111], v[60:63]
	buffer_load_dwordx4 v125, s[36:39], s51 offen lds
	v_mfma_f32_16x16x32_bf16 v[56:59], v[240:243], v[108:111], v[56:59]
	ds_read_b128 v[240:243], v121 offset:20480
	ds_read_b128 v[244:247], v121 offset:21504
	s_waitcnt lgkmcnt(8)
	v_mfma_f32_16x16x32_bf16 v[64:67], v[248:251], v[184:187], v[64:67]
	v_mfma_f32_16x16x32_bf16 v[68:71], v[252:255], v[184:187], v[68:71]
	s_mov_b32 m0, s33
	s_add_i32 s51, s50, 0x3c000
	v_mfma_f32_16x16x32_bf16 v[60:63], v[252:255], v[188:191], v[60:63]
	buffer_load_dwordx4 v125, s[36:39], s51 offen lds
	v_mfma_f32_16x16x32_bf16 v[56:59], v[248:251], v[188:191], v[56:59]
	ds_read_b128 v[248:251], v121 offset:22528
	ds_read_b128 v[252:255], v121 offset:23552
	s_setprio 2
	s_waitcnt lgkmcnt(8)
	v_mfma_f32_16x16x32_bf16 v[64:67], v[224:227], v[192:195], v[64:67]
	v_mfma_f32_16x16x32_bf16 v[68:71], v[228:231], v[192:195], v[68:71]
	s_mov_b32 m0, s34
	s_add_i32 s51, s50, 0x3e000
	v_mfma_f32_16x16x32_bf16 v[60:63], v[228:231], v[196:199], v[60:63]
	buffer_load_dwordx4 v125, s[36:39], s51 offen lds
	v_mfma_f32_16x16x32_bf16 v[56:59], v[224:227], v[196:199], v[56:59]
	ds_read_b128 v[224:227], v121 offset:24576
	ds_read_b128 v[228:231], v121 offset:25600
	s_waitcnt lgkmcnt(6)
	v_mfma_f32_16x16x32_bf16 v[64:67], v[232:235], v[200:203], v[64:67]
	v_cvt_pk_bf16_f32 v40, v80, v81
	v_mfma_f32_16x16x32_bf16 v[68:71], v[236:239], v[200:203], v[68:71]
	v_cvt_pk_bf16_f32 v41, v82, v83
	v_mfma_f32_16x16x32_bf16 v[60:63], v[236:239], v[204:207], v[60:63]
	v_cvt_pk_bf16_f32 v42, v76, v77
	v_mfma_f32_16x16x32_bf16 v[56:59], v[232:235], v[204:207], v[56:59]
	v_cvt_pk_bf16_f32 v43, v78, v79
	ds_read_b128 v[232:235], v121 offset:26624
	ds_read_b128 v[236:239], v121 offset:27648
	s_waitcnt lgkmcnt(6)
	ds_read_b128 v[152:155], v183 offset:2048
	ds_read_b128 v[156:159], v183 offset:2112
	v_mfma_f32_16x16x32_bf16 v[64:67], v[240:243], v[208:211], v[64:67]
	v_cvt_pk_bf16_f32 v44, v84, v85
	v_mfma_f32_16x16x32_bf16 v[68:71], v[244:247], v[208:211], v[68:71]
	v_cvt_pk_bf16_f32 v45, v86, v87
	v_mfma_f32_16x16x32_bf16 v[60:63], v[244:247], v[212:215], v[60:63]
	v_cvt_pk_bf16_f32 v46, v72, v73
	v_mfma_f32_16x16x32_bf16 v[56:59], v[240:243], v[212:215], v[56:59]
	v_cvt_pk_bf16_f32 v47, v74, v75
	ds_read_b128 v[240:243], v121 offset:28672
	ds_read_b128 v[244:247], v121 offset:29696
	s_waitcnt lgkmcnt(8)
	v_mfma_f32_16x16x32_bf16 v[64:67], v[248:251], v[216:219], v[64:67]
	v_pk_max_i16 v40, v40, 0
	v_mfma_f32_16x16x32_bf16 v[68:71], v[252:255], v[216:219], v[68:71]
	v_pk_max_i16 v41, v41, 0
	v_mfma_f32_16x16x32_bf16 v[60:63], v[252:255], v[220:223], v[60:63]
	v_pk_max_i16 v42, v42, 0
	v_mfma_f32_16x16x32_bf16 v[56:59], v[248:251], v[220:223], v[56:59]
	v_pk_max_i16 v43, v43, 0
	ds_read_b128 v[248:251], v121 offset:30720
	ds_read_b128 v[252:255], v121 offset:31744
	s_setprio 1
	s_waitcnt lgkmcnt(8)
	v_mfma_f32_16x16x32_bf16 v[80:83], v[224:227], v[88:91], v[160:163]
	v_pk_max_i16 v44, v44, 0
	v_mfma_f32_16x16x32_bf16 v[76:79], v[228:231], v[88:91], v[164:167]
	v_pk_max_i16 v45, v45, 0
	v_mfma_f32_16x16x32_bf16 v[72:75], v[228:231], v[92:95], v[164:167]
	v_pk_max_i16 v46, v46, 0
	v_mfma_f32_16x16x32_bf16 v[84:87], v[224:227], v[92:95], v[160:163]
	v_pk_max_i16 v47, v47, 0
	ds_read_b128 v[224:227], v121 offset:32768
	ds_read_b128 v[228:231], v121 offset:33792
	s_waitcnt lgkmcnt(8)
	v_mfma_f32_16x16x32_bf16 v[80:83], v[232:235], v[96:99], v[80:83]
	v_cvt_pk_bf16_f32 v48, v64, v65
	v_mfma_f32_16x16x32_bf16 v[76:79], v[236:239], v[96:99], v[76:79]
	v_cvt_pk_bf16_f32 v49, v66, v67
	v_mfma_f32_16x16x32_bf16 v[72:75], v[236:239], v[100:103], v[72:75]
	v_cvt_pk_bf16_f32 v50, v68, v69
	v_mfma_f32_16x16x32_bf16 v[84:87], v[232:235], v[100:103], v[84:87]
	v_cvt_pk_bf16_f32 v51, v70, v71
	ds_read_b128 v[232:235], v121 offset:34816
	ds_read_b128 v[236:239], v121 offset:35840
	s_waitcnt lgkmcnt(6)
	v_mfma_f32_16x16x32_bf16 v[80:83], v[240:243], v[104:107], v[80:83]
	v_cvt_pk_bf16_f32 v52, v56, v57
	v_mfma_f32_16x16x32_bf16 v[76:79], v[244:247], v[104:107], v[76:79]
	v_cvt_pk_bf16_f32 v53, v58, v59
	v_mfma_f32_16x16x32_bf16 v[72:75], v[244:247], v[108:111], v[72:75]
	v_cvt_pk_bf16_f32 v54, v60, v61
	v_mfma_f32_16x16x32_bf16 v[84:87], v[240:243], v[108:111], v[84:87]
	v_cvt_pk_bf16_f32 v55, v62, v63
	ds_read_b128 v[240:243], v121 offset:36864
	ds_read_b128 v[244:247], v121 offset:37888
	s_waitcnt lgkmcnt(6)
	v_mfma_f32_16x16x32_bf16 v[80:83], v[248:251], v[184:187], v[80:83]
	v_pk_max_i16 v48, v48, 0
	v_mfma_f32_16x16x32_bf16 v[76:79], v[252:255], v[184:187], v[76:79]
	v_pk_max_i16 v49, v49, 0
	v_mfma_f32_16x16x32_bf16 v[72:75], v[252:255], v[188:191], v[72:75]
	v_pk_max_i16 v50, v50, 0
	v_mfma_f32_16x16x32_bf16 v[84:87], v[248:251], v[188:191], v[84:87]
	v_pk_max_i16 v51, v51, 0
	ds_read_b128 v[248:251], v121 offset:38912
	ds_read_b128 v[252:255], v121 offset:39936
	s_setprio 0
	s_waitcnt lgkmcnt(6)
	v_mfma_f32_16x16x32_bf16 v[80:83], v[224:227], v[192:195], v[80:83]
	v_pk_max_i16 v52, v52, 0
	v_mfma_f32_16x16x32_bf16 v[76:79], v[228:231], v[192:195], v[76:79]
	v_pk_max_i16 v53, v53, 0
	v_mfma_f32_16x16x32_bf16 v[72:75], v[228:231], v[196:199], v[72:75]
	v_pk_max_i16 v54, v54, 0
	v_mfma_f32_16x16x32_bf16 v[84:87], v[224:227], v[196:199], v[84:87]
	v_pk_max_i16 v55, v55, 0
	s_waitcnt lgkmcnt(4)
	v_mfma_f32_16x16x32_bf16 v[80:83], v[232:235], v[200:203], v[80:83]
	v_mfma_f32_16x16x32_bf16 v[76:79], v[236:239], v[200:203], v[76:79]
	v_mfma_f32_16x16x32_bf16 v[72:75], v[236:239], v[204:207], v[72:75]
	v_mfma_f32_16x16x32_bf16 v[84:87], v[232:235], v[204:207], v[84:87]
	s_add_i32 s50, s50, 0x40000
	v_add_u32_e32 v183, 0x800, v183
	s_add_i32 s52, s52, 1
	s_branch .Lnerf_hid_a0

.Lnerf_hid_b0:
	s_waitcnt vmcnt(0) lgkmcnt(0)
	s_barrier
	v_mfma_f32_16x16x32_bf16 v[80:83], v[240:243], v[208:211], v[80:83]
	ds_read_b128 v[224:227], v121 offset:40960
	ds_read_b128 v[228:231], v121 offset:41984
	v_mfma_f32_16x16x32_bf16 v[76:79], v[244:247], v[208:211], v[76:79]
	ds_read_b128 v[232:235], v121 offset:43008
	v_mfma_f32_16x16x32_bf16 v[72:75], v[244:247], v[212:215], v[72:75]
	ds_read_b128 v[236:239], v121 offset:44032
	v_mfma_f32_16x16x32_bf16 v[84:87], v[240:243], v[212:215], v[84:87]
	ds_read_b128 v[240:243], v121 offset:45056
	ds_read_b128 v[244:247], v121 offset:46080
	v_mfma_f32_16x16x32_bf16 v[80:83], v[248:251], v[216:219], v[80:83]
	v_mfma_f32_16x16x32_bf16 v[76:79], v[252:255], v[216:219], v[76:79]
	v_mfma_f32_16x16x32_bf16 v[72:75], v[252:255], v[220:223], v[72:75]
	v_mfma_f32_16x16x32_bf16 v[84:87], v[248:251], v[220:223], v[84:87]
	ds_read_b128 v[248:251], v121 offset:47104
	ds_read_b128 v[252:255], v121 offset:48128
	s_setprio 3
	s_waitcnt lgkmcnt(6)
	v_mfma_f32_16x16x32_bf16 v[64:67], v[224:227], v[0:3], v[152:155]
	v_mfma_f32_16x16x32_bf16 v[68:71], v[228:231], v[0:3], v[156:159]
	v_mfma_f32_16x16x32_bf16 v[60:63], v[228:231], v[4:7], v[156:159]
	v_mfma_f32_16x16x32_bf16 v[56:59], v[224:227], v[4:7], v[152:155]
	ds_read_b128 v[224:227], v121 offset:49152
	ds_read_b128 v[228:231], v121 offset:50176
	s_waitcnt lgkmcnt(6)
	ds_read_b128 v[160:163], v183 offset:128
	ds_read_b128 v[164:167], v183 offset:192
	v_mfma_f32_16x16x32_bf16 v[64:67], v[232:235], v[12:15], v[64:67]
	v_cvt_pk_bf16_f32 v112, v80, v81
	v_mfma_f32_16x16x32_bf16 v[68:71], v[236:239], v[12:15], v[68:71]
	v_cvt_pk_bf16_f32 v113, v82, v83
	v_mfma_f32_16x16x32_bf16 v[60:63], v[236:239], v[8:11], v[60:63]
	v_cvt_pk_bf16_f32 v114, v76, v77
	v_mfma_f32_16x16x32_bf16 v[56:59], v[232:235], v[8:11], v[56:59]
	v_cvt_pk_bf16_f32 v115, v78, v79
	ds_read_b128 v[232:235], v121 offset:51200
	ds_read_b128 v[236:239], v121 offset:52224
	s_waitcnt lgkmcnt(8)
	v_mfma_f32_16x16x32_bf16 v[64:67], v[240:243], v[16:19], v[64:67]
	v_cvt_pk_bf16_f32 v116, v84, v85
	v_mfma_f32_16x16x32_bf16 v[68:71], v[244:247], v[16:19], v[68:71]
	v_cvt_pk_bf16_f32 v117, v86, v87
	v_mfma_f32_16x16x32_bf16 v[60:63], v[244:247], v[20:23], v[60:63]
	v_cvt_pk_bf16_f32 v118, v72, v73
	v_mfma_f32_16x16x32_bf16 v[56:59], v[240:243], v[20:23], v[56:59]
	v_cvt_pk_bf16_f32 v119, v74, v75
	ds_read_b128 v[240:243], v121 offset:53248
	ds_read_b128 v[244:247], v121 offset:54272
	s_waitcnt lgkmcnt(8)
	v_mfma_f32_16x16x32_bf16 v[64:67], v[248:251], v[24:27], v[64:67]
	v_pk_max_i16 v112, v112, 0
	v_mfma_f32_16x16x32_bf16 v[68:71], v[252:255], v[24:27], v[68:71]
	v_pk_max_i16 v113, v113, 0
	v_mfma_f32_16x16x32_bf16 v[60:63], v[252:255], v[28:31], v[60:63]
	v_pk_max_i16 v114, v114, 0
	v_mfma_f32_16x16x32_bf16 v[56:59], v[248:251], v[28:31], v[56:59]
	v_pk_max_i16 v115, v115, 0
	ds_read_b128 v[248:251], v121 offset:55296
	ds_read_b128 v[252:255], v121 offset:56320
	s_setprio 2
	s_waitcnt lgkmcnt(8)
	v_mfma_f32_16x16x32_bf16 v[64:67], v[224:227], v[32:35], v[64:67]
	v_pk_max_i16 v116, v116, 0
	v_mfma_f32_16x16x32_bf16 v[68:71], v[228:231], v[32:35], v[68:71]
	v_pk_max_i16 v117, v117, 0
	v_mfma_f32_16x16x32_bf16 v[60:63], v[228:231], v[36:39], v[60:63]
	v_pk_max_i16 v118, v118, 0
	v_mfma_f32_16x16x32_bf16 v[56:59], v[224:227], v[36:39], v[56:59]
	v_pk_max_i16 v119, v119, 0
	ds_read_b128 v[224:227], v121 offset:57344
	ds_read_b128 v[228:231], v121 offset:58368
	s_waitcnt lgkmcnt(6)
	v_mfma_f32_16x16x32_bf16 v[64:67], v[232:235], v[40:43], v[64:67]
	v_mfma_f32_16x16x32_bf16 v[68:71], v[236:239], v[40:43], v[68:71]
	s_mov_b32 m0, s35
	s_add_i32 s51, s50, 0x0
	v_mfma_f32_16x16x32_bf16 v[60:63], v[236:239], v[44:47], v[60:63]
	buffer_load_dwordx4 v125, s[36:39], s51 offen lds
	v_mfma_f32_16x16x32_bf16 v[56:59], v[232:235], v[44:47], v[56:59]
	ds_read_b128 v[232:235], v121 offset:59392
	ds_read_b128 v[236:239], v121 offset:60416
	s_waitcnt lgkmcnt(6)
	ds_read_b128 v[152:155], v183 offset:256
	ds_read_b128 v[156:159], v183 offset:320
	v_mfma_f32_16x16x32_bf16 v[64:67], v[240:243], v[48:51], v[64:67]
	v_mfma_f32_16x16x32_bf16 v[68:71], v[244:247], v[48:51], v[68:71]
	s_mov_b32 m0, s42
	s_add_i32 s51, s50, 0x2000
	v_mfma_f32_16x16x32_bf16 v[60:63], v[244:247], v[52:55], v[60:63]
	buffer_load_dwordx4 v125, s[36:39], s51 offen lds
	v_mfma_f32_16x16x32_bf16 v[56:59], v[240:243], v[52:55], v[56:59]
	ds_read_b128 v[240:243], v121 offset:61440
	ds_read_b128 v[244:247], v121 offset:62464
	s_waitcnt lgkmcnt(8)
	v_mfma_f32_16x16x32_bf16 v[64:67], v[248:251], v[112:115], v[64:67]
	v_mfma_f32_16x16x32_bf16 v[68:71], v[252:255], v[112:115], v[68:71]
	s_mov_b32 m0, s41
	s_add_i32 s51, s50, 0x4000
	v_mfma_f32_16x16x32_bf16 v[60:63], v[252:255], v[116:119], v[60:63]
	buffer_load_dwordx4 v125, s[36:39], s51 offen lds
	v_mfma_f32_16x16x32_bf16 v[56:59], v[248:251], v[116:119], v[56:59]
	ds_read_b128 v[248:251], v121 offset:63488
	ds_read_b128 v[252:255], v121 offset:64512
	s_setprio 1
	s_waitcnt lgkmcnt(8)
	v_mfma_f32_16x16x32_bf16 v[80:83], v[224:227], v[0:3], v[160:163]
	v_mfma_f32_16x16x32_bf16 v[76:79], v[228:231], v[0:3], v[164:167]
	s_mov_b32 m0, s40
	s_add_i32 s51, s50, 0x6000
	v_mfma_f32_16x16x32_bf16 v[72:75], v[228:231], v[4:7], v[164:167]
	buffer_load_dwordx4 v125, s[36:39], s51 offen lds
	v_mfma_f32_16x16x32_bf16 v[84:87], v[224:227], v[4:7], v[160:163]
	ds_read_b128 v[224:227], v126 offset:57344
	ds_read_b128 v[228:231], v126 offset:58368
	s_waitcnt lgkmcnt(8)
	v_mfma_f32_16x16x32_bf16 v[80:83], v[232:235], v[12:15], v[80:83]
	v_cvt_pk_bf16_f32 v88, v64, v65
	v_mfma_f32_16x16x32_bf16 v[76:79], v[236:239], v[12:15], v[76:79]
	v_cvt_pk_bf16_f32 v89, v66, v67
	v_mfma_f32_16x16x32_bf16 v[72:75], v[236:239], v[8:11], v[72:75]
	v_cvt_pk_bf16_f32 v90, v68, v69
	v_mfma_f32_16x16x32_bf16 v[84:87], v[232:235], v[8:11], v[84:87]
	v_cvt_pk_bf16_f32 v91, v70, v71
	ds_read_b128 v[232:235], v126 offset:59392
	ds_read_b128 v[236:239], v126 offset:60416
	s_waitcnt lgkmcnt(6)
	v_mfma_f32_16x16x32_bf16 v[80:83], v[240:243], v[16:19], v[80:83]
	v_cvt_pk_bf16_f32 v92, v56, v57
	v_mfma_f32_16x16x32_bf16 v[76:79], v[244:247], v[16:19], v[76:79]
	v_cvt_pk_bf16_f32 v93, v58, v59
	v_mfma_f32_16x16x32_bf16 v[72:75], v[244:247], v[20:23], v[72:75]
	v_cvt_pk_bf16_f32 v94, v60, v61
	v_mfma_f32_16x16x32_bf16 v[84:87], v[240:243], v[20:23], v[84:87]
	v_cvt_pk_bf16_f32 v95, v62, v63
	ds_read_b128 v[240:243], v126 offset:61440
	ds_read_b128 v[244:247], v126 offset:62464
	s_waitcnt lgkmcnt(6)
	v_mfma_f32_16x16x32_bf16 v[80:83], v[248:251], v[24:27], v[80:83]
	v_pk_max_i16 v88, v88, 0
	v_mfma_f32_16x16x32_bf16 v[76:79], v[252:255], v[24:27], v[76:79]
	v_pk_max_i16 v89, v89, 0
	v_mfma_f32_16x16x32_bf16 v[72:75], v[252:255], v[28:31], v[72:75]
	v_pk_max_i16 v90, v90, 0
	v_mfma_f32_16x16x32_bf16 v[84:87], v[248:251], v[28:31], v[84:87]
	v_pk_max_i16 v91, v91, 0
	ds_read_b128 v[248:251], v126 offset:63488
	ds_read_b128 v[252:255], v126 offset:64512
	s_setprio 0
	s_waitcnt lgkmcnt(6)
	v_mfma_f32_16x16x32_bf16 v[80:83], v[224:227], v[32:35], v[80:83]
	v_pk_max_i16 v92, v92, 0
	v_mfma_f32_16x16x32_bf16 v[76:79], v[228:231], v[32:35], v[76:79]
	v_pk_max_i16 v93, v93, 0
	v_mfma_f32_16x16x32_bf16 v[72:75], v[228:231], v[36:39], v[72:75]
	v_pk_max_i16 v94, v94, 0
	v_mfma_f32_16x16x32_bf16 v[84:87], v[224:227], v[36:39], v[84:87]
	v_pk_max_i16 v95, v95, 0
	s_waitcnt lgkmcnt(4)
	v_mfma_f32_16x16x32_bf16 v[80:83], v[232:235], v[40:43], v[80:83]
	v_mfma_f32_16x16x32_bf16 v[76:79], v[236:239], v[40:43], v[76:79]
	v_mfma_f32_16x16x32_bf16 v[72:75], v[236:239], v[44:47], v[72:75]
	v_mfma_f32_16x16x32_bf16 v[84:87], v[232:235], v[44:47], v[84:87]
.Lnerf_hid_b1:
	s_waitcnt vmcnt(0) lgkmcnt(0)
	s_barrier
	v_mfma_f32_16x16x32_bf16 v[80:83], v[240:243], v[48:51], v[80:83]
	ds_read_b128 v[224:227], v121 offset:8192
	ds_read_b128 v[228:231], v121 offset:9216
	v_mfma_f32_16x16x32_bf16 v[76:79], v[244:247], v[48:51], v[76:79]
	ds_read_b128 v[232:235], v121 offset:10240
	v_mfma_f32_16x16x32_bf16 v[72:75], v[244:247], v[52:55], v[72:75]
	ds_read_b128 v[236:239], v121 offset:11264
	v_mfma_f32_16x16x32_bf16 v[84:87], v[240:243], v[52:55], v[84:87]
	ds_read_b128 v[240:243], v121 offset:12288
	ds_read_b128 v[244:247], v121 offset:13312
	v_mfma_f32_16x16x32_bf16 v[80:83], v[248:251], v[112:115], v[80:83]
	v_mfma_f32_16x16x32_bf16 v[76:79], v[252:255], v[112:115], v[76:79]
	v_mfma_f32_16x16x32_bf16 v[72:75], v[252:255], v[116:119], v[72:75]
	v_mfma_f32_16x16x32_bf16 v[84:87], v[248:251], v[116:119], v[84:87]
	ds_read_b128 v[248:251], v121 offset:14336
	ds_read_b128 v[252:255], v121 offset:15360
	s_setprio 3
	s_waitcnt lgkmcnt(6)
	v_mfma_f32_16x16x32_bf16 v[64:67], v[224:227], v[0:3], v[152:155]
	v_mfma_f32_16x16x32_bf16 v[68:71], v[228:231], v[0:3], v[156:159]
	v_mfma_f32_16x16x32_bf16 v[60:63], v[228:231], v[4:7], v[156:159]
	v_mfma_f32_16x16x32_bf16 v[56:59], v[224:227], v[4:7], v[152:155]
	ds_read_b128 v[224:227], v121 offset:16384
	ds_read_b128 v[228:231], v121 offset:17408
	s_waitcnt lgkmcnt(6)
	ds_read_b128 v[160:163], v183 offset:384
	ds_read_b128 v[164:167], v183 offset:448
	v_mfma_f32_16x16x32_bf16 v[64:67], v[232:235], v[12:15], v[64:67]
	v_cvt_pk_bf16_f32 v96, v80, v81
	v_mfma_f32_16x16x32_bf16 v[68:71], v[236:239], v[12:15], v[68:71]
	v_cvt_pk_bf16_f32 v97, v82, v83
	v_mfma_f32_16x16x32_bf16 v[60:63], v[236:239], v[8:11], v[60:63]
	v_cvt_pk_bf16_f32 v98, v76, v77
	v_mfma_f32_16x16x32_bf16 v[56:59], v[232:235], v[8:11], v[56:59]
	v_cvt_pk_bf16_f32 v99, v78, v79
	ds_read_b128 v[232:235], v121 offset:18432
	ds_read_b128 v[236:239], v121 offset:19456
	s_waitcnt lgkmcnt(8)
	v_mfma_f32_16x16x32_bf16 v[64:67], v[240:243], v[16:19], v[64:67]
	v_cvt_pk_bf16_f32 v100, v84, v85
	v_mfma_f32_16x16x32_bf16 v[68:71], v[244:247], v[16:19], v[68:71]
	v_cvt_pk_bf16_f32 v101, v86, v87
	v_mfma_f32_16x16x32_bf16 v[60:63], v[244:247], v[20:23], v[60:63]
	v_cvt_pk_bf16_f32 v102, v72, v73
	v_mfma_f32_16x16x32_bf16 v[56:59], v[240:243], v[20:23], v[56:59]
	v_cvt_pk_bf16_f32 v103, v74, v75
	ds_read_b128 v[240:243], v121 offset:20480
	ds_read_b128 v[244:247], v121 offset:21504
	s_waitcnt lgkmcnt(8)
	v_mfma_f32_16x16x32_bf16 v[64:67], v[248:251], v[24:27], v[64:67]
	v_pk_max_i16 v96, v96, 0
	v_mfma_f32_16x16x32_bf16 v[68:71], v[252:255], v[24:27], v[68:71]
	v_pk_max_i16 v97, v97, 0
	v_mfma_f32_16x16x32_bf16 v[60:63], v[252:255], v[28:31], v[60:63]
	v_pk_max_i16 v98, v98, 0
	v_mfma_f32_16x16x32_bf16 v[56:59], v[248:251], v[28:31], v[56:59]
	v_pk_max_i16 v99, v99, 0
	ds_read_b128 v[248:251], v121 offset:22528
	ds_read_b128 v[252:255], v121 offset:23552
	s_setprio 2
	s_waitcnt lgkmcnt(8)
	v_mfma_f32_16x16x32_bf16 v[64:67], v[224:227], v[32:35], v[64:67]
	v_pk_max_i16 v100, v100, 0
	v_mfma_f32_16x16x32_bf16 v[68:71], v[228:231], v[32:35], v[68:71]
	v_pk_max_i16 v101, v101, 0
	v_mfma_f32_16x16x32_bf16 v[60:63], v[228:231], v[36:39], v[60:63]
	v_pk_max_i16 v102, v102, 0
	v_mfma_f32_16x16x32_bf16 v[56:59], v[224:227], v[36:39], v[56:59]
	v_pk_max_i16 v103, v103, 0
	ds_read_b128 v[224:227], v121 offset:24576
	ds_read_b128 v[228:231], v121 offset:25600
	s_waitcnt lgkmcnt(6)
	v_mfma_f32_16x16x32_bf16 v[64:67], v[232:235], v[40:43], v[64:67]
	v_mfma_f32_16x16x32_bf16 v[68:71], v[236:239], v[40:43], v[68:71]
	s_mov_b32 m0, s28
	s_add_i32 s51, s50, 0x8000
	v_mfma_f32_16x16x32_bf16 v[60:63], v[236:239], v[44:47], v[60:63]
	buffer_load_dwordx4 v125, s[36:39], s51 offen lds
	v_mfma_f32_16x16x32_bf16 v[56:59], v[232:235], v[44:47], v[56:59]
	ds_read_b128 v[232:235], v121 offset:26624
	ds_read_b128 v[236:239], v121 offset:27648
	s_waitcnt lgkmcnt(6)
	ds_read_b128 v[152:155], v183 offset:512
	ds_read_b128 v[156:159], v183 offset:576
	v_mfma_f32_16x16x32_bf16 v[64:67], v[240:243], v[48:51], v[64:67]
	v_mfma_f32_16x16x32_bf16 v[68:71], v[244:247], v[48:51], v[68:71]
	s_mov_b32 m0, s29
	s_add_i32 s51, s50, 0xa000
	v_mfma_f32_16x16x32_bf16 v[60:63], v[244:247], v[52:55], v[60:63]
	buffer_load_dwordx4 v125, s[36:39], s51 offen lds
	v_mfma_f32_16x16x32_bf16 v[56:59], v[240:243], v[52:55], v[56:59]
	ds_read_b128 v[240:243], v121 offset:28672
	ds_read_b128 v[244:247], v121 offset:29696
	s_waitcnt lgkmcnt(8)
	v_mfma_f32_16x16x32_bf16 v[64:67], v[248:251], v[112:115], v[64:67]
	v_mfma_f32_16x16x32_bf16 v[68:71], v[252:255], v[112:115], v[68:71]
	s_mov_b32 m0, s33
	s_add_i32 s51, s50, 0xc000
	v_mfma_f32_16x16x32_bf16 v[60:63], v[252:255], v[116:119], v[60:63]
	buffer_load_dwordx4 v125, s[36:39], s51 offen lds
	v_mfma_f32_16x16x32_bf16 v[56:59], v[248:251], v[116:119], v[56:59]
	ds_read_b128 v[248:251], v121 offset:30720
	ds_read_b128 v[252:255], v121 offset:31744
	s_setprio 1
	s_waitcnt lgkmcnt(8)
	v_mfma_f32_16x16x32_bf16 v[80:83], v[224:227], v[0:3], v[160:163]
	v_mfma_f32_16x16x32_bf16 v[76:79], v[228:231], v[0:3], v[164:167]
	s_mov_b32 m0, s34
	s_add_i32 s51, s50, 0xe000
	v_mfma_f32_16x16x32_bf16 v[72:75], v[228:231], v[4:7], v[164:167]
	buffer_load_dwordx4 v125, s[36:39], s51 offen lds
	v_mfma_f32_16x16x32_bf16 v[84:87], v[224:227], v[4:7], v[160:163]
	ds_read_b128 v[224:227], v121 offset:32768
	ds_read_b128 v[228:231], v121 offset:33792
	s_waitcnt lgkmcnt(8)
	v_mfma_f32_16x16x32_bf16 v[80:83], v[232:235], v[12:15], v[80:83]
	v_cvt_pk_bf16_f32 v104, v64, v65
	v_mfma_f32_16x16x32_bf16 v[76:79], v[236:239], v[12:15], v[76:79]
	v_cvt_pk_bf16_f32 v105, v66, v67
	v_mfma_f32_16x16x32_bf16 v[72:75], v[236:239], v[8:11], v[72:75]
	v_cvt_pk_bf16_f32 v106, v68, v69
	v_mfma_f32_16x16x32_bf16 v[84:87], v[232:235], v[8:11], v[84:87]
	v_cvt_pk_bf16_f32 v107, v70, v71
	ds_read_b128 v[232:235], v121 offset:34816
	ds_read_b128 v[236:239], v121 offset:35840
	s_waitcnt lgkmcnt(6)
	v_mfma_f32_16x16x32_bf16 v[80:83], v[240:243], v[16:19], v[80:83]
	v_cvt_pk_bf16_f32 v108, v56, v57
	v_mfma_f32_16x16x32_bf16 v[76:79], v[244:247], v[16:19], v[76:79]
	v_cvt_pk_bf16_f32 v109, v58, v59
	v_mfma_f32_16x16x32_bf16 v[72:75], v[244:247], v[20:23], v[72:75]
	v_cvt_pk_bf16_f32 v110, v60, v61
	v_mfma_f32_16x16x32_bf16 v[84:87], v[240:243], v[20:23], v[84:87]
	v_cvt_pk_bf16_f32 v111, v62, v63
	ds_read_b128 v[240:243], v121 offset:36864
	ds_read_b128 v[244:247], v121 offset:37888
	s_waitcnt lgkmcnt(6)
	v_mfma_f32_16x16x32_bf16 v[80:83], v[248:251], v[24:27], v[80:83]
	v_pk_max_i16 v104, v104, 0
	v_mfma_f32_16x16x32_bf16 v[76:79], v[252:255], v[24:27], v[76:79]
	v_pk_max_i16 v105, v105, 0
	v_mfma_f32_16x16x32_bf16 v[72:75], v[252:255], v[28:31], v[72:75]
	v_pk_max_i16 v106, v106, 0
	v_mfma_f32_16x16x32_bf16 v[84:87], v[248:251], v[28:31], v[84:87]
	v_pk_max_i16 v107, v107, 0
	ds_read_b128 v[248:251], v121 offset:38912
	ds_read_b128 v[252:255], v121 offset:39936
	s_setprio 0
	s_waitcnt lgkmcnt(6)
	v_mfma_f32_16x16x32_bf16 v[80:83], v[224:227], v[32:35], v[80:83]
	v_pk_max_i16 v108, v108, 0
	v_mfma_f32_16x16x32_bf16 v[76:79], v[228:231], v[32:35], v[76:79]
	v_pk_max_i16 v109, v109, 0
	v_mfma_f32_16x16x32_bf16 v[72:75], v[228:231], v[36:39], v[72:75]
	v_pk_max_i16 v110, v110, 0
	v_mfma_f32_16x16x32_bf16 v[84:87], v[224:227], v[36:39], v[84:87]
	v_pk_max_i16 v111, v111, 0
	s_waitcnt lgkmcnt(4)
	v_mfma_f32_16x16x32_bf16 v[80:83], v[232:235], v[40:43], v[80:83]
	v_mfma_f32_16x16x32_bf16 v[76:79], v[236:239], v[40:43], v[76:79]
	v_mfma_f32_16x16x32_bf16 v[72:75], v[236:239], v[44:47], v[72:75]
	v_mfma_f32_16x16x32_bf16 v[84:87], v[232:235], v[44:47], v[84:87]
.Lnerf_hid_b2:
	s_waitcnt vmcnt(0) lgkmcnt(0)
	s_barrier
	v_mfma_f32_16x16x32_bf16 v[80:83], v[240:243], v[48:51], v[80:83]
	ds_read_b128 v[224:227], v121 offset:40960
	ds_read_b128 v[228:231], v121 offset:41984
	v_mfma_f32_16x16x32_bf16 v[76:79], v[244:247], v[48:51], v[76:79]
	ds_read_b128 v[232:235], v121 offset:43008
	v_mfma_f32_16x16x32_bf16 v[72:75], v[244:247], v[52:55], v[72:75]
	ds_read_b128 v[236:239], v121 offset:44032
	v_mfma_f32_16x16x32_bf16 v[84:87], v[240:243], v[52:55], v[84:87]
	ds_read_b128 v[240:243], v121 offset:45056
	ds_read_b128 v[244:247], v121 offset:46080
	v_mfma_f32_16x16x32_bf16 v[80:83], v[248:251], v[112:115], v[80:83]
	v_mfma_f32_16x16x32_bf16 v[76:79], v[252:255], v[112:115], v[76:79]
	v_mfma_f32_16x16x32_bf16 v[72:75], v[252:255], v[116:119], v[72:75]
	v_mfma_f32_16x16x32_bf16 v[84:87], v[248:251], v[116:119], v[84:87]
	ds_read_b128 v[248:251], v121 offset:47104
	ds_read_b128 v[252:255], v121 offset:48128
	s_setprio 3
	s_waitcnt lgkmcnt(6)
	v_mfma_f32_16x16x32_bf16 v[64:67], v[224:227], v[0:3], v[152:155]
	v_mfma_f32_16x16x32_bf16 v[68:71], v[228:231], v[0:3], v[156:159]
	v_mfma_f32_16x16x32_bf16 v[60:63], v[228:231], v[4:7], v[156:159]
	v_mfma_f32_16x16x32_bf16 v[56:59], v[224:227], v[4:7], v[152:155]
	ds_read_b128 v[224:227], v121 offset:49152
	ds_read_b128 v[228:231], v121 offset:50176
	s_waitcnt lgkmcnt(6)
	ds_read_b128 v[160:163], v183 offset:640
	ds_read_b128 v[164:167], v183 offset:704
	v_mfma_f32_16x16x32_bf16 v[64:67], v[232:235], v[12:15], v[64:67]
	v_cvt_pk_bf16_f32 v184, v80, v81
	v_mfma_f32_16x16x32_bf16 v[68:71], v[236:239], v[12:15], v[68:71]
	v_cvt_pk_bf16_f32 v185, v82, v83
	v_mfma_f32_16x16x32_bf16 v[60:63], v[236:239], v[8:11], v[60:63]
	v_cvt_pk_bf16_f32 v186, v76, v77
	v_mfma_f32_16x16x32_bf16 v[56:59], v[232:235], v[8:11], v[56:59]
	v_cvt_pk_bf16_f32 v187, v78, v79
	ds_read_b128 v[232:235], v121 offset:51200
	ds_read_b128 v[236:239], v121 offset:52224
	s_waitcnt lgkmcnt(8)
	v_mfma_f32_16x16x32_bf16 v[64:67], v[240:243], v[16:19], v[64:67]
	v_cvt_pk_bf16_f32 v188, v84, v85
	v_mfma_f32_16x16x32_bf16 v[68:71], v[244:247], v[16:19], v[68:71]
	v_cvt_pk_bf16_f32 v189, v86, v87
	v_mfma_f32_16x16x32_bf16 v[60:63], v[244:247], v[20:23], v[60:63]
	v_cvt_pk_bf16_f32 v190, v72, v73
	v_mfma_f32_16x16x32_bf16 v[56:59], v[240:243], v[20:23], v[56:59]
	v_cvt_pk_bf16_f32 v191, v74, v75
	ds_read_b128 v[240:243], v121 offset:53248
	ds_read_b128 v[244:247], v121 offset:54272
	s_waitcnt lgkmcnt(8)
	v_mfma_f32_16x16x32_bf16 v[64:67], v[248:251], v[24:27], v[64:67]
	v_pk_max_i16 v184, v184, 0
	v_mfma_f32_16x16x32_bf16 v[68:71], v[252:255], v[24:27], v[68:71]
	v_pk_max_i16 v185, v185, 0
	v_mfma_f32_16x16x32_bf16 v[60:63], v[252:255], v[28:31], v[60:63]
	v_pk_max_i16 v186, v186, 0
	v_mfma_f32_16x16x32_bf16 v[56:59], v[248:251], v[28:31], v[56:59]
	v_pk_max_i16 v187, v187, 0
	ds_read_b128 v[248:251], v121 offset:55296
	ds_read_b128 v[252:255], v121 offset:56320
	s_setprio 2
	s_waitcnt lgkmcnt(8)
	v_mfma_f32_16x16x32_bf16 v[64:67], v[224:227], v[32:35], v[64:67]
	v_pk_max_i16 v188, v188, 0
	v_mfma_f32_16x16x32_bf16 v[68:71], v[228:231], v[32:35], v[68:71]
	v_pk_max_i16 v189, v189, 0
	v_mfma_f32_16x16x32_bf16 v[60:63], v[228:231], v[36:39], v[60:63]
	v_pk_max_i16 v190, v190, 0
	v_mfma_f32_16x16x32_bf16 v[56:59], v[224:227], v[36:39], v[56:59]
	v_pk_max_i16 v191, v191, 0
	ds_read_b128 v[224:227], v121 offset:57344
	ds_read_b128 v[228:231], v121 offset:58368
	s_waitcnt lgkmcnt(6)
	v_mfma_f32_16x16x32_bf16 v[64:67], v[232:235], v[40:43], v[64:67]
	v_mfma_f32_16x16x32_bf16 v[68:71], v[236:239], v[40:43], v[68:71]
	s_mov_b32 m0, s35
	s_add_i32 s51, s50, 0x10000
	v_mfma_f32_16x16x32_bf16 v[60:63], v[236:239], v[44:47], v[60:63]
	buffer_load_dwordx4 v125, s[36:39], s51 offen lds
	v_mfma_f32_16x16x32_bf16 v[56:59], v[232:235], v[44:47], v[56:59]
	ds_read_b128 v[232:235], v121 offset:59392
	ds_read_b128 v[236:239], v121 offset:60416
	s_waitcnt lgkmcnt(6)
	ds_read_b128 v[152:155], v183 offset:768
	ds_read_b128 v[156:159], v183 offset:832
	v_mfma_f32_16x16x32_bf16 v[64:67], v[240:243], v[48:51], v[64:67]
	v_mfma_f32_16x16x32_bf16 v[68:71], v[244:247], v[48:51], v[68:71]
	s_mov_b32 m0, s42
	s_add_i32 s51, s50, 0x12000
	v_mfma_f32_16x16x32_bf16 v[60:63], v[244:247], v[52:55], v[60:63]
	buffer_load_dwordx4 v125, s[36:39], s51 offen lds
	v_mfma_f32_16x16x32_bf16 v[56:59], v[240:243], v[52:55], v[56:59]
	ds_read_b128 v[240:243], v121 offset:61440
	ds_read_b128 v[244:247], v121 offset:62464
	s_waitcnt lgkmcnt(8)
	v_mfma_f32_16x16x32_bf16 v[64:67], v[248:251], v[112:115], v[64:67]
	v_mfma_f32_16x16x32_bf16 v[68:71], v[252:255], v[112:115], v[68:71]
	s_mov_b32 m0, s41
	s_add_i32 s51, s50, 0x14000
	v_mfma_f32_16x16x32_bf16 v[60:63], v[252:255], v[116:119], v[60:63]
	buffer_load_dwordx4 v125, s[36:39], s51 offen lds
	v_mfma_f32_16x16x32_bf16 v[56:59], v[248:251], v[116:119], v[56:59]
	ds_read_b128 v[248:251], v121 offset:63488
	ds_read_b128 v[252:255], v121 offset:64512
	s_setprio 1
	s_waitcnt lgkmcnt(8)
	v_mfma_f32_16x16x32_bf16 v[80:83], v[224:227], v[0:3], v[160:163]
	v_mfma_f32_16x16x32_bf16 v[76:79], v[228:231], v[0:3], v[164:167]
	s_mov_b32 m0, s40
	s_add_i32 s51, s50, 0x16000
	v_mfma_f32_16x16x32_bf16 v[72:75], v[228:231], v[4:7], v[164:167]
	buffer_load_dwordx4 v125, s[36:39], s51 offen lds
	v_mfma_f32_16x16x32_bf16 v[84:87], v[224:227], v[4:7], v[160:163]
	ds_read_b128 v[224:227], v126 offset:57344
	ds_read_b128 v[228:231], v126 offset:58368
	s_waitcnt lgkmcnt(8)
	v_mfma_f32_16x16x32_bf16 v[80:83], v[232:235], v[12:15], v[80:83]
	v_cvt_pk_bf16_f32 v192, v64, v65
	v_mfma_f32_16x16x32_bf16 v[76:79], v[236:239], v[12:15], v[76:79]
	v_cvt_pk_bf16_f32 v193, v66, v67
	v_mfma_f32_16x16x32_bf16 v[72:75], v[236:239], v[8:11], v[72:75]
	v_cvt_pk_bf16_f32 v194, v68, v69
	v_mfma_f32_16x16x32_bf16 v[84:87], v[232:235], v[8:11], v[84:87]
	v_cvt_pk_bf16_f32 v195, v70, v71
	ds_read_b128 v[232:235], v126 offset:59392
	ds_read_b128 v[236:239], v126 offset:60416
	s_waitcnt lgkmcnt(6)
	v_mfma_f32_16x16x32_bf16 v[80:83], v[240:243], v[16:19], v[80:83]
	v_cvt_pk_bf16_f32 v196, v56, v57
	v_mfma_f32_16x16x32_bf16 v[76:79], v[244:247], v[16:19], v[76:79]
	v_cvt_pk_bf16_f32 v197, v58, v59
	v_mfma_f32_16x16x32_bf16 v[72:75], v[244:247], v[20:23], v[72:75]
	v_cvt_pk_bf16_f32 v198, v60, v61
	v_mfma_f32_16x16x32_bf16 v[84:87], v[240:243], v[20:23], v[84:87]
	v_cvt_pk_bf16_f32 v199, v62, v63
	ds_read_b128 v[240:243], v126 offset:61440
	ds_read_b128 v[244:247], v126 offset:62464
	s_waitcnt lgkmcnt(6)
	v_mfma_f32_16x16x32_bf16 v[80:83], v[248:251], v[24:27], v[80:83]
	v_pk_max_i16 v192, v192, 0
	v_mfma_f32_16x16x32_bf16 v[76:79], v[252:255], v[24:27], v[76:79]
	v_pk_max_i16 v193, v193, 0
	v_mfma_f32_16x16x32_bf16 v[72:75], v[252:255], v[28:31], v[72:75]
	v_pk_max_i16 v194, v194, 0
	v_mfma_f32_16x16x32_bf16 v[84:87], v[248:251], v[28:31], v[84:87]
	v_pk_max_i16 v195, v195, 0
	ds_read_b128 v[248:251], v126 offset:63488
	ds_read_b128 v[252:255], v126 offset:64512
	s_setprio 0
	s_waitcnt lgkmcnt(6)
	v_mfma_f32_16x16x32_bf16 v[80:83], v[224:227], v[32:35], v[80:83]
	v_pk_max_i16 v196, v196, 0
	v_mfma_f32_16x16x32_bf16 v[76:79], v[228:231], v[32:35], v[76:79]
	v_pk_max_i16 v197, v197, 0
	v_mfma_f32_16x16x32_bf16 v[72:75], v[228:231], v[36:39], v[72:75]
	v_pk_max_i16 v198, v198, 0
	v_mfma_f32_16x16x32_bf16 v[84:87], v[224:227], v[36:39], v[84:87]
	v_pk_max_i16 v199, v199, 0
	s_waitcnt lgkmcnt(4)
	v_mfma_f32_16x16x32_bf16 v[80:83], v[232:235], v[40:43], v[80:83]
	v_mfma_f32_16x16x32_bf16 v[76:79], v[236:239], v[40:43], v[76:79]
	v_mfma_f32_16x16x32_bf16 v[72:75], v[236:239], v[44:47], v[72:75]
	v_mfma_f32_16x16x32_bf16 v[84:87], v[232:235], v[44:47], v[84:87]
.Lnerf_hid_b3:
	s_waitcnt vmcnt(0) lgkmcnt(0)
	s_barrier
	v_mfma_f32_16x16x32_bf16 v[80:83], v[240:243], v[48:51], v[80:83]
	ds_read_b128 v[224:227], v121 offset:8192
	ds_read_b128 v[228:231], v121 offset:9216
	v_mfma_f32_16x16x32_bf16 v[76:79], v[244:247], v[48:51], v[76:79]
	ds_read_b128 v[232:235], v121 offset:10240
	v_mfma_f32_16x16x32_bf16 v[72:75], v[244:247], v[52:55], v[72:75]
	ds_read_b128 v[236:239], v121 offset:11264
	v_mfma_f32_16x16x32_bf16 v[84:87], v[240:243], v[52:55], v[84:87]
	ds_read_b128 v[240:243], v121 offset:12288
	ds_read_b128 v[244:247], v121 offset:13312
	v_mfma_f32_16x16x32_bf16 v[80:83], v[248:251], v[112:115], v[80:83]
	v_mfma_f32_16x16x32_bf16 v[76:79], v[252:255], v[112:115], v[76:79]
	v_mfma_f32_16x16x32_bf16 v[72:75], v[252:255], v[116:119], v[72:75]
	v_mfma_f32_16x16x32_bf16 v[84:87], v[248:251], v[116:119], v[84:87]
	ds_read_b128 v[248:251], v121 offset:14336
	ds_read_b128 v[252:255], v121 offset:15360
	s_setprio 3
	s_waitcnt lgkmcnt(6)
	v_mfma_f32_16x16x32_bf16 v[64:67], v[224:227], v[0:3], v[152:155]
	v_mfma_f32_16x16x32_bf16 v[68:71], v[228:231], v[0:3], v[156:159]
	v_mfma_f32_16x16x32_bf16 v[60:63], v[228:231], v[4:7], v[156:159]
	v_mfma_f32_16x16x32_bf16 v[56:59], v[224:227], v[4:7], v[152:155]
	ds_read_b128 v[224:227], v121 offset:16384
	ds_read_b128 v[228:231], v121 offset:17408
	s_waitcnt lgkmcnt(6)
	ds_read_b128 v[160:163], v183 offset:896
	ds_read_b128 v[164:167], v183 offset:960
	v_mfma_f32_16x16x32_bf16 v[64:67], v[232:235], v[12:15], v[64:67]
	v_cvt_pk_bf16_f32 v200, v80, v81
	v_mfma_f32_16x16x32_bf16 v[68:71], v[236:239], v[12:15], v[68:71]
	v_cvt_pk_bf16_f32 v201, v82, v83
	v_mfma_f32_16x16x32_bf16 v[60:63], v[236:239], v[8:11], v[60:63]
	v_cvt_pk_bf16_f32 v202, v76, v77
	v_mfma_f32_16x16x32_bf16 v[56:59], v[232:235], v[8:11], v[56:59]
	v_cvt_pk_bf16_f32 v203, v78, v79
	ds_read_b128 v[232:235], v121 offset:18432
	ds_read_b128 v[236:239], v121 offset:19456
	s_waitcnt lgkmcnt(8)
	v_mfma_f32_16x16x32_bf16 v[64:67], v[240:243], v[16:19], v[64:67]
	v_cvt_pk_bf16_f32 v204, v84, v85
	v_mfma_f32_16x16x32_bf16 v[68:71], v[244:247], v[16:19], v[68:71]
	v_cvt_pk_bf16_f32 v205, v86, v87
	v_mfma_f32_16x16x32_bf16 v[60:63], v[244:247], v[20:23], v[60:63]
	v_cvt_pk_bf16_f32 v206, v72, v73
	v_mfma_f32_16x16x32_bf16 v[56:59], v[240:243], v[20:23], v[56:59]
	v_cvt_pk_bf16_f32 v207, v74, v75
	ds_read_b128 v[240:243], v121 offset:20480
	ds_read_b128 v[244:247], v121 offset:21504
	s_waitcnt lgkmcnt(8)
	v_mfma_f32_16x16x32_bf16 v[64:67], v[248:251], v[24:27], v[64:67]
	v_pk_max_i16 v200, v200, 0
	v_mfma_f32_16x16x32_bf16 v[68:71], v[252:255], v[24:27], v[68:71]
	v_pk_max_i16 v201, v201, 0
	v_mfma_f32_16x16x32_bf16 v[60:63], v[252:255], v[28:31], v[60:63]
	v_pk_max_i16 v202, v202, 0
	v_mfma_f32_16x16x32_bf16 v[56:59], v[248:251], v[28:31], v[56:59]
	v_pk_max_i16 v203, v203, 0
	ds_read_b128 v[248:251], v121 offset:22528
	ds_read_b128 v[252:255], v121 offset:23552
	s_setprio 2
	s_waitcnt lgkmcnt(8)
	v_mfma_f32_16x16x32_bf16 v[64:67], v[224:227], v[32:35], v[64:67]
	v_pk_max_i16 v204, v204, 0
	v_mfma_f32_16x16x32_bf16 v[68:71], v[228:231], v[32:35], v[68:71]
	v_pk_max_i16 v205, v205, 0
	v_mfma_f32_16x16x32_bf16 v[60:63], v[228:231], v[36:39], v[60:63]
	v_pk_max_i16 v206, v206, 0
	v_mfma_f32_16x16x32_bf16 v[56:59], v[224:227], v[36:39], v[56:59]
	v_pk_max_i16 v207, v207, 0
	ds_read_b128 v[224:227], v121 offset:24576
	ds_read_b128 v[228:231], v121 offset:25600
	s_waitcnt lgkmcnt(6)
	v_mfma_f32_16x16x32_bf16 v[64:67], v[232:235], v[40:43], v[64:67]
	v_mfma_f32_16x16x32_bf16 v[68:71], v[236:239], v[40:43], v[68:71]
	s_mov_b32 m0, s28
	s_add_i32 s51, s50, 0x18000
	v_mfma_f32_16x16x32_bf16 v[60:63], v[236:239], v[44:47], v[60:63]
	buffer_load_dwordx4 v125, s[36:39], s51 offen lds
	v_mfma_f32_16x16x32_bf16 v[56:59], v[232:235], v[44:47], v[56:59]
	ds_read_b128 v[232:235], v121 offset:26624
	ds_read_b128 v[236:239], v121 offset:27648
	s_waitcnt lgkmcnt(6)
	ds_read_b128 v[152:155], v183 offset:1024
	ds_read_b128 v[156:159], v183 offset:1088
	v_mfma_f32_16x16x32_bf16 v[64:67], v[240:243], v[48:51], v[64:67]
	v_mfma_f32_16x16x32_bf16 v[68:71], v[244:247], v[48:51], v[68:71]
	s_mov_b32 m0, s29
	s_add_i32 s51, s50, 0x1a000
	v_mfma_f32_16x16x32_bf16 v[60:63], v[244:247], v[52:55], v[60:63]
	buffer_load_dwordx4 v125, s[36:39], s51 offen lds
	v_mfma_f32_16x16x32_bf16 v[56:59], v[240:243], v[52:55], v[56:59]
	ds_read_b128 v[240:243], v121 offset:28672
	ds_read_b128 v[244:247], v121 offset:29696
	s_waitcnt lgkmcnt(8)
	v_mfma_f32_16x16x32_bf16 v[64:67], v[248:251], v[112:115], v[64:67]
	v_mfma_f32_16x16x32_bf16 v[68:71], v[252:255], v[112:115], v[68:71]
	s_mov_b32 m0, s33
	s_add_i32 s51, s50, 0x1c000
	v_mfma_f32_16x16x32_bf16 v[60:63], v[252:255], v[116:119], v[60:63]
	buffer_load_dwordx4 v125, s[36:39], s51 offen lds
	v_mfma_f32_16x16x32_bf16 v[56:59], v[248:251], v[116:119], v[56:59]
	ds_read_b128 v[248:251], v121 offset:30720
	ds_read_b128 v[252:255], v121 offset:31744
	s_setprio 1
	s_waitcnt lgkmcnt(8)
	v_mfma_f32_16x16x32_bf16 v[80:83], v[224:227], v[0:3], v[160:163]
	v_mfma_f32_16x16x32_bf16 v[76:79], v[228:231], v[0:3], v[164:167]
	s_mov_b32 m0, s34
	s_add_i32 s51, s50, 0x1e000
	v_mfma_f32_16x16x32_bf16 v[72:75], v[228:231], v[4:7], v[164:167]
	buffer_load_dwordx4 v125, s[36:39], s51 offen lds
	v_mfma_f32_16x16x32_bf16 v[84:87], v[224:227], v[4:7], v[160:163]
	ds_read_b128 v[224:227], v121 offset:32768
	ds_read_b128 v[228:231], v121 offset:33792
	s_waitcnt lgkmcnt(8)
	v_mfma_f32_16x16x32_bf16 v[80:83], v[232:235], v[12:15], v[80:83]
	v_cvt_pk_bf16_f32 v208, v64, v65
	v_mfma_f32_16x16x32_bf16 v[76:79], v[236:239], v[12:15], v[76:79]
	v_cvt_pk_bf16_f32 v209, v66, v67
	v_mfma_f32_16x16x32_bf16 v[72:75], v[236:239], v[8:11], v[72:75]
	v_cvt_pk_bf16_f32 v210, v68, v69
	v_mfma_f32_16x16x32_bf16 v[84:87], v[232:235], v[8:11], v[84:87]
	v_cvt_pk_bf16_f32 v211, v70, v71
	ds_read_b128 v[232:235], v121 offset:34816
	ds_read_b128 v[236:239], v121 offset:35840
	s_waitcnt lgkmcnt(6)
	v_mfma_f32_16x16x32_bf16 v[80:83], v[240:243], v[16:19], v[80:83]
	v_cvt_pk_bf16_f32 v212, v56, v57
	v_mfma_f32_16x16x32_bf16 v[76:79], v[244:247], v[16:19], v[76:79]
	v_cvt_pk_bf16_f32 v213, v58, v59
	v_mfma_f32_16x16x32_bf16 v[72:75], v[244:247], v[20:23], v[72:75]
	v_cvt_pk_bf16_f32 v214, v60, v61
	v_mfma_f32_16x16x32_bf16 v[84:87], v[240:243], v[20:23], v[84:87]
	v_cvt_pk_bf16_f32 v215, v62, v63
	ds_read_b128 v[240:243], v121 offset:36864
	ds_read_b128 v[244:247], v121 offset:37888
	s_waitcnt lgkmcnt(6)
	v_mfma_f32_16x16x32_bf16 v[80:83], v[248:251], v[24:27], v[80:83]
	v_pk_max_i16 v208, v208, 0
	v_mfma_f32_16x16x32_bf16 v[76:79], v[252:255], v[24:27], v[76:79]
	v_pk_max_i16 v209, v209, 0
	v_mfma_f32_16x16x32_bf16 v[72:75], v[252:255], v[28:31], v[72:75]
	v_pk_max_i16 v210, v210, 0
	v_mfma_f32_16x16x32_bf16 v[84:87], v[248:251], v[28:31], v[84:87]
	v_pk_max_i16 v211, v211, 0
	ds_read_b128 v[248:251], v121 offset:38912
	ds_read_b128 v[252:255], v121 offset:39936
	s_setprio 0
	s_waitcnt lgkmcnt(6)
	v_mfma_f32_16x16x32_bf16 v[80:83], v[224:227], v[32:35], v[80:83]
	v_pk_max_i16 v212, v212, 0
	v_mfma_f32_16x16x32_bf16 v[76:79], v[228:231], v[32:35], v[76:79]
	v_pk_max_i16 v213, v213, 0
	v_mfma_f32_16x16x32_bf16 v[72:75], v[228:231], v[36:39], v[72:75]
	v_pk_max_i16 v214, v214, 0
	v_mfma_f32_16x16x32_bf16 v[84:87], v[224:227], v[36:39], v[84:87]
	v_pk_max_i16 v215, v215, 0
	s_waitcnt lgkmcnt(4)
	v_mfma_f32_16x16x32_bf16 v[80:83], v[232:235], v[40:43], v[80:83]
	v_mfma_f32_16x16x32_bf16 v[76:79], v[236:239], v[40:43], v[76:79]
	v_mfma_f32_16x16x32_bf16 v[72:75], v[236:239], v[44:47], v[72:75]
	v_mfma_f32_16x16x32_bf16 v[84:87], v[232:235], v[44:47], v[84:87]
	s_cmp_eq_u32 s52, 3
	s_cbranch_scc1 .Lnerf_head
.Lnerf_hid_b4:
	s_waitcnt vmcnt(0) lgkmcnt(0)
	s_barrier
	v_mfma_f32_16x16x32_bf16 v[80:83], v[240:243], v[48:51], v[80:83]
	ds_read_b128 v[224:227], v121 offset:40960
	ds_read_b128 v[228:231], v121 offset:41984
	v_mfma_f32_16x16x32_bf16 v[76:79], v[244:247], v[48:51], v[76:79]
	ds_read_b128 v[232:235], v121 offset:43008
	v_mfma_f32_16x16x32_bf16 v[72:75], v[244:247], v[52:55], v[72:75]
	ds_read_b128 v[236:239], v121 offset:44032
	v_mfma_f32_16x16x32_bf16 v[84:87], v[240:243], v[52:55], v[84:87]
	ds_read_b128 v[240:243], v121 offset:45056
	ds_read_b128 v[244:247], v121 offset:46080
	v_mfma_f32_16x16x32_bf16 v[80:83], v[248:251], v[112:115], v[80:83]
	v_mfma_f32_16x16x32_bf16 v[76:79], v[252:255], v[112:115], v[76:79]
	v_mfma_f32_16x16x32_bf16 v[72:75], v[252:255], v[116:119], v[72:75]
	v_mfma_f32_16x16x32_bf16 v[84:87], v[248:251], v[116:119], v[84:87]
	ds_read_b128 v[248:251], v121 offset:47104
	ds_read_b128 v[252:255], v121 offset:48128
	s_setprio 3
	s_waitcnt lgkmcnt(6)
	v_mfma_f32_16x16x32_bf16 v[64:67], v[224:227], v[88:91], v[152:155]
	v_mfma_f32_16x16x32_bf16 v[68:71], v[228:231], v[88:91], v[156:159]
	v_mfma_f32_16x16x32_bf16 v[60:63], v[228:231], v[92:95], v[156:159]
	v_mfma_f32_16x16x32_bf16 v[56:59], v[224:227], v[92:95], v[152:155]
	ds_read_b128 v[224:227], v121 offset:49152
	ds_read_b128 v[228:231], v121 offset:50176
	s_waitcnt lgkmcnt(6)
	ds_read_b128 v[160:163], v183 offset:1152
	ds_read_b128 v[164:167], v183 offset:1216
	v_mfma_f32_16x16x32_bf16 v[64:67], v[232:235], v[96:99], v[64:67]
	v_cvt_pk_bf16_f32 v216, v80, v81
	v_mfma_f32_16x16x32_bf16 v[68:71], v[236:239], v[96:99], v[68:71]
	v_cvt_pk_bf16_f32 v217, v82, v83
	v_mfma_f32_16x16x32_bf16 v[60:63], v[236:239], v[100:103], v[60:63]
	v_cvt_pk_bf16_f32 v218, v76, v77
	v_mfma_f32_16x16x32_bf16 v[56:59], v[232:235], v[100:103], v[56:59]
	v_cvt_pk_bf16_f32 v219, v78, v79
	ds_read_b128 v[232:235], v121 offset:51200
	ds_read_b128 v[236:239], v121 offset:52224
	s_waitcnt lgkmcnt(8)
	v_mfma_f32_16x16x32_bf16 v[64:67], v[240:243], v[104:107], v[64:67]
	v_cvt_pk_bf16_f32 v220, v84, v85
	v_mfma_f32_16x16x32_bf16 v[68:71], v[244:247], v[104:107], v[68:71]
	v_cvt_pk_bf16_f32 v221, v86, v87
	v_mfma_f32_16x16x32_bf16 v[60:63], v[244:247], v[108:111], v[60:63]
	v_cvt_pk_bf16_f32 v222, v72, v73
	v_mfma_f32_16x16x32_bf16 v[56:59], v[240:243], v[108:111], v[56:59]
	v_cvt_pk_bf16_f32 v223, v74, v75
	ds_read_b128 v[240:243], v121 offset:53248
	ds_read_b128 v[244:247], v121 offset:54272
	s_waitcnt lgkmcnt(8)
	v_mfma_f32_16x16x32_bf16 v[64:67], v[248:251], v[184:187], v[64:67]
	v_pk_max_i16 v216, v216, 0
	v_mfma_f32_16x16x32_bf16 v[68:71], v[252:255], v[184:187], v[68:71]
	v_pk_max_i16 v217, v217, 0
	v_mfma_f32_16x16x32_bf16 v[60:63], v[252:255], v[188:191], v[60:63]
	v_pk_max_i16 v218, v218, 0
	v_mfma_f32_16x16x32_bf16 v[56:59], v[248:251], v[188:191], v[56:59]
	v_pk_max_i16 v219, v219, 0
	ds_read_b128 v[248:251], v121 offset:55296
	ds_read_b128 v[252:255], v121 offset:56320
	s_setprio 2
	s_waitcnt lgkmcnt(8)
	v_mfma_f32_16x16x32_bf16 v[64:67], v[224:227], v[192:195], v[64:67]
	v_pk_max_i16 v220, v220, 0
	v_mfma_f32_16x16x32_bf16 v[68:71], v[228:231], v[192:195], v[68:71]
	v_pk_max_i16 v221, v221, 0
	v_mfma_f32_16x16x32_bf16 v[60:63], v[228:231], v[196:199], v[60:63]
	v_pk_max_i16 v222, v222, 0
	v_mfma_f32_16x16x32_bf16 v[56:59], v[224:227], v[196:199], v[56:59]
	v_pk_max_i16 v223, v223, 0
	ds_read_b128 v[224:227], v121 offset:57344
	ds_read_b128 v[228:231], v121 offset:58368
	s_waitcnt lgkmcnt(6)
	v_mfma_f32_16x16x32_bf16 v[64:67], v[232:235], v[200:203], v[64:67]
	v_mfma_f32_16x16x32_bf16 v[68:71], v[236:239], v[200:203], v[68:71]
	s_mov_b32 m0, s35
	s_add_i32 s51, s50, 0x20000
	v_mfma_f32_16x16x32_bf16 v[60:63], v[236:239], v[204:207], v[60:63]
	buffer_load_dwordx4 v125, s[36:39], s51 offen lds
	v_mfma_f32_16x16x32_bf16 v[56:59], v[232:235], v[204:207], v[56:59]
	ds_read_b128 v[232:235], v121 offset:59392
	ds_read_b128 v[236:239], v121 offset:60416
	s_waitcnt lgkmcnt(6)
	ds_read_b128 v[152:155], v183 offset:1280
	ds_read_b128 v[156:159], v183 offset:1344
	v_mfma_f32_16x16x32_bf16 v[64:67], v[240:243], v[208:211], v[64:67]
	v_mfma_f32_16x16x32_bf16 v[68:71], v[244:247], v[208:211], v[68:71]
	s_mov_b32 m0, s42
	s_add_i32 s51, s50, 0x22000
	v_mfma_f32_16x16x32_bf16 v[60:63], v[244:247], v[212:215], v[60:63]
	buffer_load_dwordx4 v125, s[36:39], s51 offen lds
	v_mfma_f32_16x16x32_bf16 v[56:59], v[240:243], v[212:215], v[56:59]
	ds_read_b128 v[240:243], v121 offset:61440
	ds_read_b128 v[244:247], v121 offset:62464
	s_waitcnt lgkmcnt(8)
	v_mfma_f32_16x16x32_bf16 v[64:67], v[248:251], v[216:219], v[64:67]
	v_mfma_f32_16x16x32_bf16 v[68:71], v[252:255], v[216:219], v[68:71]
	s_mov_b32 m0, s41
	s_add_i32 s51, s50, 0x24000
	v_mfma_f32_16x16x32_bf16 v[60:63], v[252:255], v[220:223], v[60:63]
	buffer_load_dwordx4 v125, s[36:39], s51 offen lds
	v_mfma_f32_16x16x32_bf16 v[56:59], v[248:251], v[220:223], v[56:59]
	ds_read_b128 v[248:251], v121 offset:63488
	ds_read_b128 v[252:255], v121 offset:64512
	s_setprio 1
	s_waitcnt lgkmcnt(8)
	v_mfma_f32_16x16x32_bf16 v[80:83], v[224:227], v[88:91], v[160:163]
	v_mfma_f32_16x16x32_bf16 v[76:79], v[228:231], v[88:91], v[164:167]
	s_mov_b32 m0, s40
	s_add_i32 s51, s50, 0x26000
	v_mfma_f32_16x16x32_bf16 v[72:75], v[228:231], v[92:95], v[164:167]
	buffer_load_dwordx4 v125, s[36:39], s51 offen lds
	v_mfma_f32_16x16x32_bf16 v[84:87], v[224:227], v[92:95], v[160:163]
	ds_read_b128 v[224:227], v126 offset:57344
	ds_read_b128 v[228:231], v126 offset:58368
	s_waitcnt lgkmcnt(8)
	v_mfma_f32_16x16x32_bf16 v[80:83], v[232:235], v[96:99], v[80:83]
	v_cvt_pk_bf16_f32 v0, v64, v65
	v_mfma_f32_16x16x32_bf16 v[76:79], v[236:239], v[96:99], v[76:79]
	v_cvt_pk_bf16_f32 v1, v66, v67
	v_mfma_f32_16x16x32_bf16 v[72:75], v[236:239], v[100:103], v[72:75]
	v_cvt_pk_bf16_f32 v2, v68, v69
	v_mfma_f32_16x16x32_bf16 v[84:87], v[232:235], v[100:103], v[84:87]
	v_cvt_pk_bf16_f32 v3, v70, v71
	ds_read_b128 v[232:235], v126 offset:59392
	ds_read_b128 v[236:239], v126 offset:60416
	s_waitcnt lgkmcnt(6)
	v_mfma_f32_16x16x32_bf16 v[80:83], v[240:243], v[104:107], v[80:83]
	v_cvt_pk_bf16_f32 v4, v56, v57
	v_mfma_f32_16x16x32_bf16 v[76:79], v[244:247], v[104:107], v[76:79]
	v_cvt_pk_bf16_f32 v5, v58, v59
	v_mfma_f32_16x16x32_bf16 v[72:75], v[244:247], v[108:111], v[72:75]
	v_cvt_pk_bf16_f32 v6, v60, v61
	v_mfma_f32_16x16x32_bf16 v[84:87], v[240:243], v[108:111], v[84:87]
	v_cvt_pk_bf16_f32 v7, v62, v63
	ds_read_b128 v[240:243], v126 offset:61440
	ds_read_b128 v[244:247], v126 offset:62464
	s_waitcnt lgkmcnt(6)
	v_mfma_f32_16x16x32_bf16 v[80:83], v[248:251], v[184:187], v[80:83]
	v_pk_max_i16 v0, v0, 0
	v_mfma_f32_16x16x32_bf16 v[76:79], v[252:255], v[184:187], v[76:79]
	v_pk_max_i16 v1, v1, 0
	v_mfma_f32_16x16x32_bf16 v[72:75], v[252:255], v[188:191], v[72:75]
	v_pk_max_i16 v2, v2, 0
	v_mfma_f32_16x16x32_bf16 v[84:87], v[248:251], v[188:191], v[84:87]
	v_pk_max_i16 v3, v3, 0
	ds_read_b128 v[248:251], v126 offset:63488
	ds_read_b128 v[252:255], v126 offset:64512
	s_setprio 0
	s_waitcnt lgkmcnt(6)
	v_mfma_f32_16x16x32_bf16 v[80:83], v[224:227], v[192:195], v[80:83]
	v_pk_max_i16 v4, v4, 0
	v_mfma_f32_16x16x32_bf16 v[76:79], v[228:231], v[192:195], v[76:79]
	v_pk_max_i16 v5, v5, 0
	v_mfma_f32_16x16x32_bf16 v[72:75], v[228:231], v[196:199], v[72:75]
	v_pk_max_i16 v6, v6, 0
	v_mfma_f32_16x16x32_bf16 v[84:87], v[224:227], v[196:199], v[84:87]
	v_pk_max_i16 v7, v7, 0
	s_waitcnt lgkmcnt(4)
	v_mfma_f32_16x16x32_bf16 v[80:83], v[232:235], v[200:203], v[80:83]
	v_mfma_f32_16x16x32_bf16 v[76:79], v[236:239], v[200:203], v[76:79]
	v_mfma_f32_16x16x32_bf16 v[72:75], v[236:239], v[204:207], v[72:75]
	v_mfma_f32_16x16x32_bf16 v[84:87], v[232:235], v[204:207], v[84:87]
.Lnerf_hid_b5:
	s_waitcnt vmcnt(0) lgkmcnt(0)
	s_barrier
	v_mfma_f32_16x16x32_bf16 v[80:83], v[240:243], v[208:211], v[80:83]
	ds_read_b128 v[224:227], v121 offset:8192
	ds_read_b128 v[228:231], v121 offset:9216
	v_mfma_f32_16x16x32_bf16 v[76:79], v[244:247], v[208:211], v[76:79]
	ds_read_b128 v[232:235], v121 offset:10240
	v_mfma_f32_16x16x32_bf16 v[72:75], v[244:247], v[212:215], v[72:75]
	ds_read_b128 v[236:239], v121 offset:11264
	v_mfma_f32_16x16x32_bf16 v[84:87], v[240:243], v[212:215], v[84:87]
	ds_read_b128 v[240:243], v121 offset:12288
	ds_read_b128 v[244:247], v121 offset:13312
	v_mfma_f32_16x16x32_bf16 v[80:83], v[248:251], v[216:219], v[80:83]
	v_mfma_f32_16x16x32_bf16 v[76:79], v[252:255], v[216:219], v[76:79]
	v_mfma_f32_16x16x32_bf16 v[72:75], v[252:255], v[220:223], v[72:75]
	v_mfma_f32_16x16x32_bf16 v[84:87], v[248:251], v[220:223], v[84:87]
	ds_read_b128 v[248:251], v121 offset:14336
	ds_read_b128 v[252:255], v121 offset:15360
	s_setprio 3
	s_waitcnt lgkmcnt(6)
	v_mfma_f32_16x16x32_bf16 v[64:67], v[224:227], v[88:91], v[152:155]
	v_mfma_f32_16x16x32_bf16 v[68:71], v[228:231], v[88:91], v[156:159]
	v_mfma_f32_16x16x32_bf16 v[60:63], v[228:231], v[92:95], v[156:159]
	v_mfma_f32_16x16x32_bf16 v[56:59], v[224:227], v[92:95], v[152:155]
	ds_read_b128 v[224:227], v121 offset:16384
	ds_read_b128 v[228:231], v121 offset:17408
	s_waitcnt lgkmcnt(6)
	ds_read_b128 v[160:163], v183 offset:1408
	ds_read_b128 v[164:167], v183 offset:1472
	v_mfma_f32_16x16x32_bf16 v[64:67], v[232:235], v[96:99], v[64:67]
	v_cvt_pk_bf16_f32 v12, v80, v81
	v_mfma_f32_16x16x32_bf16 v[68:71], v[236:239], v[96:99], v[68:71]
	v_cvt_pk_bf16_f32 v13, v82, v83
	v_mfma_f32_16x16x32_bf16 v[60:63], v[236:239], v[100:103], v[60:63]
	v_cvt_pk_bf16_f32 v14, v76, v77
	v_mfma_f32_16x16x32_bf16 v[56:59], v[232:235], v[100:103], v[56:59]
	v_cvt_pk_bf16_f32 v15, v78, v79
	ds_read_b128 v[232:235], v121 offset:18432
	ds_read_b128 v[236:239], v121 offset:19456
	s_waitcnt lgkmcnt(8)
	v_mfma_f32_16x16x32_bf16 v[64:67], v[240:243], v[104:107], v[64:67]
	v_cvt_pk_bf16_f32 v8, v84, v85
	v_mfma_f32_16x16x32_bf16 v[68:71], v[244:247], v[104:107], v[68:71]
	v_cvt_pk_bf16_f32 v9, v86, v87
	v_mfma_f32_16x16x32_bf16 v[60:63], v[244:247], v[108:111], v[60:63]
	v_cvt_pk_bf16_f32 v10, v72, v73
	v_mfma_f32_16x16x32_bf16 v[56:59], v[240:243], v[108:111], v[56:59]
	v_cvt_pk_bf16_f32 v11, v74, v75
	ds_read_b128 v[240:243], v121 offset:20480
	ds_read_b128 v[244:247], v121 offset:21504
	s_waitcnt lgkmcnt(8)
	v_mfma_f32_16x16x32_bf16 v[64:67], v[248:251], v[184:187], v[64:67]
	v_pk_max_i16 v12, v12, 0
	v_mfma_f32_16x16x32_bf16 v[68:71], v[252:255], v[184:187], v[68:71]
	v_pk_max_i16 v13, v13, 0
	v_mfma_f32_16x16x32_bf16 v[60:63], v[252:255], v[188:191], v[60:63]
	v_pk_max_i16 v14, v14, 0
	v_mfma_f32_16x16x32_bf16 v[56:59], v[248:251], v[188:191], v[56:59]
	v_pk_max_i16 v15, v15, 0
	ds_read_b128 v[248:251], v121 offset:22528
	ds_read_b128 v[252:255], v121 offset:23552
	s_setprio 2
	s_waitcnt lgkmcnt(8)
	v_mfma_f32_16x16x32_bf16 v[64:67], v[224:227], v[192:195], v[64:67]
	v_pk_max_i16 v8, v8, 0
	v_mfma_f32_16x16x32_bf16 v[68:71], v[228:231], v[192:195], v[68:71]
	v_pk_max_i16 v9, v9, 0
	v_mfma_f32_16x16x32_bf16 v[60:63], v[228:231], v[196:199], v[60:63]
	v_pk_max_i16 v10, v10, 0
	v_mfma_f32_16x16x32_bf16 v[56:59], v[224:227], v[196:199], v[56:59]
	v_pk_max_i16 v11, v11, 0
	ds_read_b128 v[224:227], v121 offset:24576
	ds_read_b128 v[228:231], v121 offset:25600
	s_waitcnt lgkmcnt(6)
	v_mfma_f32_16x16x32_bf16 v[64:67], v[232:235], v[200:203], v[64:67]
	v_mfma_f32_16x16x32_bf16 v[68:71], v[236:239], v[200:203], v[68:71]
	s_mov_b32 m0, s28
	s_add_i32 s51, s50, 0x28000
	v_mfma_f32_16x16x32_bf16 v[60:63], v[236:239], v[204:207], v[60:63]
	buffer_load_dwordx4 v125, s[36:39], s51 offen lds
	v_mfma_f32_16x16x32_bf16 v[56:59], v[232:235], v[204:207], v[56:59]
	ds_read_b128 v[232:235], v121 offset:26624
	ds_read_b128 v[236:239], v121 offset:27648
	s_waitcnt lgkmcnt(6)
	ds_read_b128 v[152:155], v183 offset:1536
	ds_read_b128 v[156:159], v183 offset:1600
	v_mfma_f32_16x16x32_bf16 v[64:67], v[240:243], v[208:211], v[64:67]
	v_mfma_f32_16x16x32_bf16 v[68:71], v[244:247], v[208:211], v[68:71]
	s_mov_b32 m0, s29
	s_add_i32 s51, s50, 0x2a000
	v_mfma_f32_16x16x32_bf16 v[60:63], v[244:247], v[212:215], v[60:63]
	buffer_load_dwordx4 v125, s[36:39], s51 offen lds
	v_mfma_f32_16x16x32_bf16 v[56:59], v[240:243], v[212:215], v[56:59]
	ds_read_b128 v[240:243], v121 offset:28672
	ds_read_b128 v[244:247], v121 offset:29696
	s_waitcnt lgkmcnt(8)
	v_mfma_f32_16x16x32_bf16 v[64:67], v[248:251], v[216:219], v[64:67]
	v_mfma_f32_16x16x32_bf16 v[68:71], v[252:255], v[216:219], v[68:71]
	s_mov_b32 m0, s33
	s_add_i32 s51, s50, 0x2c000
	v_mfma_f32_16x16x32_bf16 v[60:63], v[252:255], v[220:223], v[60:63]
	buffer_load_dwordx4 v125, s[36:39], s51 offen lds
	v_mfma_f32_16x16x32_bf16 v[56:59], v[248:251], v[220:223], v[56:59]
	ds_read_b128 v[248:251], v121 offset:30720
	ds_read_b128 v[252:255], v121 offset:31744
	s_setprio 1
	s_waitcnt lgkmcnt(8)
	v_mfma_f32_16x16x32_bf16 v[80:83], v[224:227], v[88:91], v[160:163]
	v_mfma_f32_16x16x32_bf16 v[76:79], v[228:231], v[88:91], v[164:167]
	s_mov_b32 m0, s34
	s_add_i32 s51, s50, 0x2e000
	v_mfma_f32_16x16x32_bf16 v[72:75], v[228:231], v[92:95], v[164:167]
	buffer_load_dwordx4 v125, s[36:39], s51 offen lds
	v_mfma_f32_16x16x32_bf16 v[84:87], v[224:227], v[92:95], v[160:163]
	ds_read_b128 v[224:227], v121 offset:32768
	ds_read_b128 v[228:231], v121 offset:33792
	s_waitcnt lgkmcnt(8)
	v_mfma_f32_16x16x32_bf16 v[80:83], v[232:235], v[96:99], v[80:83]
	v_cvt_pk_bf16_f32 v16, v64, v65
	v_mfma_f32_16x16x32_bf16 v[76:79], v[236:239], v[96:99], v[76:79]
	v_cvt_pk_bf16_f32 v17, v66, v67
	v_mfma_f32_16x16x32_bf16 v[72:75], v[236:239], v[100:103], v[72:75]
	v_cvt_pk_bf16_f32 v18, v68, v69
	v_mfma_f32_16x16x32_bf16 v[84:87], v[232:235], v[100:103], v[84:87]
	v_cvt_pk_bf16_f32 v19, v70, v71
	ds_read_b128 v[232:235], v121 offset:34816
	ds_read_b128 v[236:239], v121 offset:35840
	s_waitcnt lgkmcnt(6)
	v_mfma_f32_16x16x32_bf16 v[80:83], v[240:243], v[104:107], v[80:83]
	v_cvt_pk_bf16_f32 v20, v56, v57
	v_mfma_f32_16x16x32_bf16 v[76:79], v[244:247], v[104:107], v[76:79]
	v_cvt_pk_bf16_f32 v21, v58, v59
	v_mfma_f32_16x16x32_bf16 v[72:75], v[244:247], v[108:111], v[72:75]
	v_cvt_pk_bf16_f32 v22, v60, v61
	v_mfma_f32_16x16x32_bf16 v[84:87], v[240:243], v[108:111], v[84:87]
	v_cvt_pk_bf16_f32 v23, v62, v63
	ds_read_b128 v[240:243], v121 offset:36864
	ds_read_b128 v[244:247], v121 offset:37888
	s_waitcnt lgkmcnt(6)
	v_mfma_f32_16x16x32_bf16 v[80:83], v[248:251], v[184:187], v[80:83]
	v_pk_max_i16 v16, v16, 0
	v_mfma_f32_16x16x32_bf16 v[76:79], v[252:255], v[184:187], v[76:79]
	v_pk_max_i16 v17, v17, 0
	v_mfma_f32_16x16x32_bf16 v[72:75], v[252:255], v[188:191], v[72:75]
	v_pk_max_i16 v18, v18, 0
	v_mfma_f32_16x16x32_bf16 v[84:87], v[248:251], v[188:191], v[84:87]
	v_pk_max_i16 v19, v19, 0
	ds_read_b128 v[248:251], v121 offset:38912
	ds_read_b128 v[252:255], v121 offset:39936
	s_setprio 0
	s_waitcnt lgkmcnt(6)
	v_mfma_f32_16x16x32_bf16 v[80:83], v[224:227], v[192:195], v[80:83]
	v_pk_max_i16 v20, v20, 0
	v_mfma_f32_16x16x32_bf16 v[76:79], v[228:231], v[192:195], v[76:79]
	v_pk_max_i16 v21, v21, 0
	v_mfma_f32_16x16x32_bf16 v[72:75], v[228:231], v[196:199], v[72:75]
	v_pk_max_i16 v22, v22, 0
	v_mfma_f32_16x16x32_bf16 v[84:87], v[224:227], v[196:199], v[84:87]
	v_pk_max_i16 v23, v23, 0
	s_waitcnt lgkmcnt(4)
	v_mfma_f32_16x16x32_bf16 v[80:83], v[232:235], v[200:203], v[80:83]
	v_mfma_f32_16x16x32_bf16 v[76:79], v[236:239], v[200:203], v[76:79]
	v_mfma_f32_16x16x32_bf16 v[72:75], v[236:239], v[204:207], v[72:75]
	v_mfma_f32_16x16x32_bf16 v[84:87], v[232:235], v[204:207], v[84:87]
.Lnerf_hid_b6:
	s_waitcnt vmcnt(0) lgkmcnt(0)
	s_barrier
	v_mfma_f32_16x16x32_bf16 v[80:83], v[240:243], v[208:211], v[80:83]
	ds_read_b128 v[224:227], v121 offset:40960
	ds_read_b128 v[228:231], v121 offset:41984
	v_mfma_f32_16x16x32_bf16 v[76:79], v[244:247], v[208:211], v[76:79]
	ds_read_b128 v[232:235], v121 offset:43008
	v_mfma_f32_16x16x32_bf16 v[72:75], v[244:247], v[212:215], v[72:75]
	ds_read_b128 v[236:239], v121 offset:44032
	v_mfma_f32_16x16x32_bf16 v[84:87], v[240:243], v[212:215], v[84:87]
	ds_read_b128 v[240:243], v121 offset:45056
	ds_read_b128 v[244:247], v121 offset:46080
	v_mfma_f32_16x16x32_bf16 v[80:83], v[248:251], v[216:219], v[80:83]
	v_mfma_f32_16x16x32_bf16 v[76:79], v[252:255], v[216:219], v[76:79]
	v_mfma_f32_16x16x32_bf16 v[72:75], v[252:255], v[220:223], v[72:75]
	v_mfma_f32_16x16x32_bf16 v[84:87], v[248:251], v[220:223], v[84:87]
	ds_read_b128 v[248:251], v121 offset:47104
	ds_read_b128 v[252:255], v121 offset:48128
	s_setprio 3
	s_waitcnt lgkmcnt(6)
	v_mfma_f32_16x16x32_bf16 v[64:67], v[224:227], v[88:91], v[152:155]
	v_mfma_f32_16x16x32_bf16 v[68:71], v[228:231], v[88:91], v[156:159]
	v_mfma_f32_16x16x32_bf16 v[60:63], v[228:231], v[92:95], v[156:159]
	v_mfma_f32_16x16x32_bf16 v[56:59], v[224:227], v[92:95], v[152:155]
	ds_read_b128 v[224:227], v121 offset:49152
	ds_read_b128 v[228:231], v121 offset:50176
	s_waitcnt lgkmcnt(6)
	ds_read_b128 v[160:163], v183 offset:1664
	ds_read_b128 v[164:167], v183 offset:1728
	v_mfma_f32_16x16x32_bf16 v[64:67], v[232:235], v[96:99], v[64:67]
	v_cvt_pk_bf16_f32 v24, v80, v81
	v_mfma_f32_16x16x32_bf16 v[68:71], v[236:239], v[96:99], v[68:71]
	v_cvt_pk_bf16_f32 v25, v82, v83
	v_mfma_f32_16x16x32_bf16 v[60:63], v[236:239], v[100:103], v[60:63]
	v_cvt_pk_bf16_f32 v26, v76, v77
	v_mfma_f32_16x16x32_bf16 v[56:59], v[232:235], v[100:103], v[56:59]
	v_cvt_pk_bf16_f32 v27, v78, v79
	ds_read_b128 v[232:235], v121 offset:51200
	ds_read_b128 v[236:239], v121 offset:52224
	s_waitcnt lgkmcnt(8)
	v_mfma_f32_16x16x32_bf16 v[64:67], v[240:243], v[104:107], v[64:67]
	v_cvt_pk_bf16_f32 v28, v84, v85
	v_mfma_f32_16x16x32_bf16 v[68:71], v[244:247], v[104:107], v[68:71]
	v_cvt_pk_bf16_f32 v29, v86, v87
	v_mfma_f32_16x16x32_bf16 v[60:63], v[244:247], v[108:111], v[60:63]
	v_cvt_pk_bf16_f32 v30, v72, v73
	v_mfma_f32_16x16x32_bf16 v[56:59], v[240:243], v[108:111], v[56:59]
	v_cvt_pk_bf16_f32 v31, v74, v75
	ds_read_b128 v[240:243], v121 offset:53248
	ds_read_b128 v[244:247], v121 offset:54272
	s_waitcnt lgkmcnt(8)
	v_mfma_f32_16x16x32_bf16 v[64:67], v[248:251], v[184:187], v[64:67]
	v_pk_max_i16 v24, v24, 0
	v_mfma_f32_16x16x32_bf16 v[68:71], v[252:255], v[184:187], v[68:71]
	v_pk_max_i16 v25, v25, 0
	v_mfma_f32_16x16x32_bf16 v[60:63], v[252:255], v[188:191], v[60:63]
	v_pk_max_i16 v26, v26, 0
	v_mfma_f32_16x16x32_bf16 v[56:59], v[248:251], v[188:191], v[56:59]
	v_pk_max_i16 v27, v27, 0
	ds_read_b128 v[248:251], v121 offset:55296
	ds_read_b128 v[252:255], v121 offset:56320
	s_setprio 2
	s_waitcnt lgkmcnt(8)
	v_mfma_f32_16x16x32_bf16 v[64:67], v[224:227], v[192:195], v[64:67]
	v_pk_max_i16 v28, v28, 0
	v_mfma_f32_16x16x32_bf16 v[68:71], v[228:231], v[192:195], v[68:71]
	v_pk_max_i16 v29, v29, 0
	v_mfma_f32_16x16x32_bf16 v[60:63], v[228:231], v[196:199], v[60:63]
	v_pk_max_i16 v30, v30, 0
	v_mfma_f32_16x16x32_bf16 v[56:59], v[224:227], v[196:199], v[56:59]
	v_pk_max_i16 v31, v31, 0
	ds_read_b128 v[224:227], v121 offset:57344
	ds_read_b128 v[228:231], v121 offset:58368
	s_waitcnt lgkmcnt(6)
	v_mfma_f32_16x16x32_bf16 v[64:67], v[232:235], v[200:203], v[64:67]
	v_mfma_f32_16x16x32_bf16 v[68:71], v[236:239], v[200:203], v[68:71]
	s_mov_b32 m0, s35
	s_add_i32 s51, s50, 0x30000
	v_mfma_f32_16x16x32_bf16 v[60:63], v[236:239], v[204:207], v[60:63]
	buffer_load_dwordx4 v125, s[36:39], s51 offen lds
	v_mfma_f32_16x16x32_bf16 v[56:59], v[232:235], v[204:207], v[56:59]
	ds_read_b128 v[232:235], v121 offset:59392
	ds_read_b128 v[236:239], v121 offset:60416
	s_waitcnt lgkmcnt(6)
	ds_read_b128 v[152:155], v183 offset:1792
	ds_read_b128 v[156:159], v183 offset:1856
	v_mfma_f32_16x16x32_bf16 v[64:67], v[240:243], v[208:211], v[64:67]
	v_mfma_f32_16x16x32_bf16 v[68:71], v[244:247], v[208:211], v[68:71]
	s_mov_b32 m0, s42
	s_add_i32 s51, s50, 0x32000
	v_mfma_f32_16x16x32_bf16 v[60:63], v[244:247], v[212:215], v[60:63]
	buffer_load_dwordx4 v125, s[36:39], s51 offen lds
	v_mfma_f32_16x16x32_bf16 v[56:59], v[240:243], v[212:215], v[56:59]
	ds_read_b128 v[240:243], v121 offset:61440
	ds_read_b128 v[244:247], v121 offset:62464
	s_waitcnt lgkmcnt(8)
	v_mfma_f32_16x16x32_bf16 v[64:67], v[248:251], v[216:219], v[64:67]
	v_mfma_f32_16x16x32_bf16 v[68:71], v[252:255], v[216:219], v[68:71]
	s_mov_b32 m0, s41
	s_add_i32 s51, s50, 0x34000
	v_mfma_f32_16x16x32_bf16 v[60:63], v[252:255], v[220:223], v[60:63]
	buffer_load_dwordx4 v125, s[36:39], s51 offen lds
	v_mfma_f32_16x16x32_bf16 v[56:59], v[248:251], v[220:223], v[56:59]
	ds_read_b128 v[248:251], v121 offset:63488
	ds_read_b128 v[252:255], v121 offset:64512
	s_setprio 1
	s_waitcnt lgkmcnt(8)
	v_mfma_f32_16x16x32_bf16 v[80:83], v[224:227], v[88:91], v[160:163]
	v_mfma_f32_16x16x32_bf16 v[76:79], v[228:231], v[88:91], v[164:167]
	s_mov_b32 m0, s40
	s_add_i32 s51, s50, 0x36000
	v_mfma_f32_16x16x32_bf16 v[72:75], v[228:231], v[92:95], v[164:167]
	buffer_load_dwordx4 v125, s[36:39], s51 offen lds
	v_mfma_f32_16x16x32_bf16 v[84:87], v[224:227], v[92:95], v[160:163]
	ds_read_b128 v[224:227], v126 offset:57344
	ds_read_b128 v[228:231], v126 offset:58368
	s_waitcnt lgkmcnt(8)
	v_mfma_f32_16x16x32_bf16 v[80:83], v[232:235], v[96:99], v[80:83]
	v_cvt_pk_bf16_f32 v32, v64, v65
	v_mfma_f32_16x16x32_bf16 v[76:79], v[236:239], v[96:99], v[76:79]
	v_cvt_pk_bf16_f32 v33, v66, v67
	v_mfma_f32_16x16x32_bf16 v[72:75], v[236:239], v[100:103], v[72:75]
	v_cvt_pk_bf16_f32 v34, v68, v69
	v_mfma_f32_16x16x32_bf16 v[84:87], v[232:235], v[100:103], v[84:87]
	v_cvt_pk_bf16_f32 v35, v70, v71
	ds_read_b128 v[232:235], v126 offset:59392
	ds_read_b128 v[236:239], v126 offset:60416
	s_waitcnt lgkmcnt(6)
	v_mfma_f32_16x16x32_bf16 v[80:83], v[240:243], v[104:107], v[80:83]
	v_cvt_pk_bf16_f32 v36, v56, v57
	v_mfma_f32_16x16x32_bf16 v[76:79], v[244:247], v[104:107], v[76:79]
	v_cvt_pk_bf16_f32 v37, v58, v59
	v_mfma_f32_16x16x32_bf16 v[72:75], v[244:247], v[108:111], v[72:75]
	v_cvt_pk_bf16_f32 v38, v60, v61
	v_mfma_f32_16x16x32_bf16 v[84:87], v[240:243], v[108:111], v[84:87]
	v_cvt_pk_bf16_f32 v39, v62, v63
	ds_read_b128 v[240:243], v126 offset:61440
	ds_read_b128 v[244:247], v126 offset:62464
	s_waitcnt lgkmcnt(6)
	v_mfma_f32_16x16x32_bf16 v[80:83], v[248:251], v[184:187], v[80:83]
	v_pk_max_i16 v32, v32, 0
	v_mfma_f32_16x16x32_bf16 v[76:79], v[252:255], v[184:187], v[76:79]
	v_pk_max_i16 v33, v33, 0
	v_mfma_f32_16x16x32_bf16 v[72:75], v[252:255], v[188:191], v[72:75]
	v_pk_max_i16 v34, v34, 0
	v_mfma_f32_16x16x32_bf16 v[84:87], v[248:251], v[188:191], v[84:87]
	v_pk_max_i16 v35, v35, 0
	ds_read_b128 v[248:251], v126 offset:63488
	ds_read_b128 v[252:255], v126 offset:64512
	s_setprio 0
	s_waitcnt lgkmcnt(6)
	v_mfma_f32_16x16x32_bf16 v[80:83], v[224:227], v[192:195], v[80:83]
	v_pk_max_i16 v36, v36, 0
	v_mfma_f32_16x16x32_bf16 v[76:79], v[228:231], v[192:195], v[76:79]
	v_pk_max_i16 v37, v37, 0
	v_mfma_f32_16x16x32_bf16 v[72:75], v[228:231], v[196:199], v[72:75]
	v_pk_max_i16 v38, v38, 0
	v_mfma_f32_16x16x32_bf16 v[84:87], v[224:227], v[196:199], v[84:87]
	v_pk_max_i16 v39, v39, 0
	s_waitcnt lgkmcnt(4)
	v_mfma_f32_16x16x32_bf16 v[80:83], v[232:235], v[200:203], v[80:83]
	v_mfma_f32_16x16x32_bf16 v[76:79], v[236:239], v[200:203], v[76:79]
	v_mfma_f32_16x16x32_bf16 v[72:75], v[236:239], v[204:207], v[72:75]
	v_mfma_f32_16x16x32_bf16 v[84:87], v[232:235], v[204:207], v[84:87]
.Lnerf_hid_b7:
	s_waitcnt vmcnt(0) lgkmcnt(0)
	s_barrier
	v_mfma_f32_16x16x32_bf16 v[80:83], v[240:243], v[208:211], v[80:83]
	ds_read_b128 v[224:227], v121 offset:8192
	ds_read_b128 v[228:231], v121 offset:9216
	v_mfma_f32_16x16x32_bf16 v[76:79], v[244:247], v[208:211], v[76:79]
	ds_read_b128 v[232:235], v121 offset:10240
	v_mfma_f32_16x16x32_bf16 v[72:75], v[244:247], v[212:215], v[72:75]
	ds_read_b128 v[236:239], v121 offset:11264
	v_mfma_f32_16x16x32_bf16 v[84:87], v[240:243], v[212:215], v[84:87]
	ds_read_b128 v[240:243], v121 offset:12288
	ds_read_b128 v[244:247], v121 offset:13312
	v_mfma_f32_16x16x32_bf16 v[80:83], v[248:251], v[216:219], v[80:83]
	v_mfma_f32_16x16x32_bf16 v[76:79], v[252:255], v[216:219], v[76:79]
	v_mfma_f32_16x16x32_bf16 v[72:75], v[252:255], v[220:223], v[72:75]
	v_mfma_f32_16x16x32_bf16 v[84:87], v[248:251], v[220:223], v[84:87]
	ds_read_b128 v[248:251], v121 offset:14336
	ds_read_b128 v[252:255], v121 offset:15360
	s_setprio 3
	s_waitcnt lgkmcnt(6)
	v_mfma_f32_16x16x32_bf16 v[64:67], v[224:227], v[88:91], v[152:155]
	v_mfma_f32_16x16x32_bf16 v[68:71], v[228:231], v[88:91], v[156:159]
	v_mfma_f32_16x16x32_bf16 v[60:63], v[228:231], v[92:95], v[156:159]
	v_mfma_f32_16x16x32_bf16 v[56:59], v[224:227], v[92:95], v[152:155]
	ds_read_b128 v[224:227], v121 offset:16384
	ds_read_b128 v[228:231], v121 offset:17408
	s_waitcnt lgkmcnt(6)
	ds_read_b128 v[160:163], v183 offset:1920
	ds_read_b128 v[164:167], v183 offset:1984
	v_mfma_f32_16x16x32_bf16 v[64:67], v[232:235], v[96:99], v[64:67]
	v_cvt_pk_bf16_f32 v40, v80, v81
	v_mfma_f32_16x16x32_bf16 v[68:71], v[236:239], v[96:99], v[68:71]
	v_cvt_pk_bf16_f32 v41, v82, v83
	v_mfma_f32_16x16x32_bf16 v[60:63], v[236:239], v[100:103], v[60:63]
	v_cvt_pk_bf16_f32 v42, v76, v77
	v_mfma_f32_16x16x32_bf16 v[56:59], v[232:235], v[100:103], v[56:59]
	v_cvt_pk_bf16_f32 v43, v78, v79
	ds_read_b128 v[232:235], v121 offset:18432
	ds_read_b128 v[236:239], v121 offset:19456
	s_waitcnt lgkmcnt(8)
	v_mfma_f32_16x16x32_bf16 v[64:67], v[240:243], v[104:107], v[64:67]
	v_cvt_pk_bf16_f32 v44, v84, v85
	v_mfma_f32_16x16x32_bf16 v[68:71], v[244:247], v[104:107], v[68:71]
	v_cvt_pk_bf16_f32 v45, v86, v87
	v_mfma_f32_16x16x32_bf16 v[60:63], v[244:247], v[108:111], v[60:63]
	v_cvt_pk_bf16_f32 v46, v72, v73
	v_mfma_f32_16x16x32_bf16 v[56:59], v[240:243], v[108:111], v[56:59]
	v_cvt_pk_bf16_f32 v47, v74, v75
	ds_read_b128 v[240:243], v121 offset:20480
	ds_read_b128 v[244:247], v121 offset:21504
	s_waitcnt lgkmcnt(8)
	v_mfma_f32_16x16x32_bf16 v[64:67], v[248:251], v[184:187], v[64:67]
	v_pk_max_i16 v40, v40, 0
	v_mfma_f32_16x16x32_bf16 v[68:71], v[252:255], v[184:187], v[68:71]
	v_pk_max_i16 v41, v41, 0
	v_mfma_f32_16x16x32_bf16 v[60:63], v[252:255], v[188:191], v[60:63]
	v_pk_max_i16 v42, v42, 0
	v_mfma_f32_16x16x32_bf16 v[56:59], v[248:251], v[188:191], v[56:59]
	v_pk_max_i16 v43, v43, 0
	ds_read_b128 v[248:251], v121 offset:22528
	ds_read_b128 v[252:255], v121 offset:23552
	s_setprio 2
	s_waitcnt lgkmcnt(8)
	v_mfma_f32_16x16x32_bf16 v[64:67], v[224:227], v[192:195], v[64:67]
	v_pk_max_i16 v44, v44, 0
	v_mfma_f32_16x16x32_bf16 v[68:71], v[228:231], v[192:195], v[68:71]
	v_pk_max_i16 v45, v45, 0
	v_mfma_f32_16x16x32_bf16 v[60:63], v[228:231], v[196:199], v[60:63]
	v_pk_max_i16 v46, v46, 0
	v_mfma_f32_16x16x32_bf16 v[56:59], v[224:227], v[196:199], v[56:59]
	v_pk_max_i16 v47, v47, 0
	ds_read_b128 v[224:227], v121 offset:24576
	ds_read_b128 v[228:231], v121 offset:25600
	s_waitcnt lgkmcnt(6)
	v_mfma_f32_16x16x32_bf16 v[64:67], v[232:235], v[200:203], v[64:67]
	v_mfma_f32_16x16x32_bf16 v[68:71], v[236:239], v[200:203], v[68:71]
	s_mov_b32 m0, s28
	s_add_i32 s51, s50, 0x38000
	v_mfma_f32_16x16x32_bf16 v[60:63], v[236:239], v[204:207], v[60:63]
	buffer_load_dwordx4 v125, s[36:39], s51 offen lds
	v_mfma_f32_16x16x32_bf16 v[56:59], v[232:235], v[204:207], v[56:59]
	ds_read_b128 v[232:235], v121 offset:26624
	ds_read_b128 v[236:239], v121 offset:27648
	s_waitcnt lgkmcnt(6)
	ds_read_b128 v[152:155], v183 offset:2048
	ds_read_b128 v[156:159], v183 offset:2112
	v_mfma_f32_16x16x32_bf16 v[64:67], v[240:243], v[208:211], v[64:67]
	v_mfma_f32_16x16x32_bf16 v[68:71], v[244:247], v[208:211], v[68:71]
	s_mov_b32 m0, s29
	s_add_i32 s51, s50, 0x3a000
	v_mfma_f32_16x16x32_bf16 v[60:63], v[244:247], v[212:215], v[60:63]
	buffer_load_dwordx4 v125, s[36:39], s51 offen lds
	v_mfma_f32_16x16x32_bf16 v[56:59], v[240:243], v[212:215], v[56:59]
	ds_read_b128 v[240:243], v121 offset:28672
	ds_read_b128 v[244:247], v121 offset:29696
	s_waitcnt lgkmcnt(8)
	v_mfma_f32_16x16x32_bf16 v[64:67], v[248:251], v[216:219], v[64:67]
	v_mfma_f32_16x16x32_bf16 v[68:71], v[252:255], v[216:219], v[68:71]
	s_mov_b32 m0, s33
	s_add_i32 s51, s50, 0x3c000
	v_mfma_f32_16x16x32_bf16 v[60:63], v[252:255], v[220:223], v[60:63]
	buffer_load_dwordx4 v125, s[36:39], s51 offen lds
	v_mfma_f32_16x16x32_bf16 v[56:59], v[248:251], v[220:223], v[56:59]
	ds_read_b128 v[248:251], v121 offset:30720
	ds_read_b128 v[252:255], v121 offset:31744
	s_setprio 1
	s_waitcnt lgkmcnt(8)
	v_mfma_f32_16x16x32_bf16 v[80:83], v[224:227], v[88:91], v[160:163]
	v_mfma_f32_16x16x32_bf16 v[76:79], v[228:231], v[88:91], v[164:167]
	s_mov_b32 m0, s34
	s_add_i32 s51, s50, 0x3e000
	v_mfma_f32_16x16x32_bf16 v[72:75], v[228:231], v[92:95], v[164:167]
	buffer_load_dwordx4 v125, s[36:39], s51 offen lds
	v_mfma_f32_16x16x32_bf16 v[84:87], v[224:227], v[92:95], v[160:163]
	ds_read_b128 v[224:227], v121 offset:32768
	ds_read_b128 v[228:231], v121 offset:33792
	s_waitcnt lgkmcnt(8)
	v_mfma_f32_16x16x32_bf16 v[80:83], v[232:235], v[96:99], v[80:83]
	v_cvt_pk_bf16_f32 v48, v64, v65
	v_mfma_f32_16x16x32_bf16 v[76:79], v[236:239], v[96:99], v[76:79]
	v_cvt_pk_bf16_f32 v49, v66, v67
	v_mfma_f32_16x16x32_bf16 v[72:75], v[236:239], v[100:103], v[72:75]
	v_cvt_pk_bf16_f32 v50, v68, v69
	v_mfma_f32_16x16x32_bf16 v[84:87], v[232:235], v[100:103], v[84:87]
	v_cvt_pk_bf16_f32 v51, v70, v71
	ds_read_b128 v[232:235], v121 offset:34816
	ds_read_b128 v[236:239], v121 offset:35840
	s_waitcnt lgkmcnt(6)
	v_mfma_f32_16x16x32_bf16 v[80:83], v[240:243], v[104:107], v[80:83]
	v_cvt_pk_bf16_f32 v52, v56, v57
	v_mfma_f32_16x16x32_bf16 v[76:79], v[244:247], v[104:107], v[76:79]
	v_cvt_pk_bf16_f32 v53, v58, v59
	v_mfma_f32_16x16x32_bf16 v[72:75], v[244:247], v[108:111], v[72:75]
	v_cvt_pk_bf16_f32 v54, v60, v61
	v_mfma_f32_16x16x32_bf16 v[84:87], v[240:243], v[108:111], v[84:87]
	v_cvt_pk_bf16_f32 v55, v62, v63
	ds_read_b128 v[240:243], v121 offset:36864
	ds_read_b128 v[244:247], v121 offset:37888
	s_waitcnt lgkmcnt(6)
	v_mfma_f32_16x16x32_bf16 v[80:83], v[248:251], v[184:187], v[80:83]
	v_pk_max_i16 v48, v48, 0
	v_mfma_f32_16x16x32_bf16 v[76:79], v[252:255], v[184:187], v[76:79]
	v_pk_max_i16 v49, v49, 0
	v_mfma_f32_16x16x32_bf16 v[72:75], v[252:255], v[188:191], v[72:75]
	v_pk_max_i16 v50, v50, 0
	v_mfma_f32_16x16x32_bf16 v[84:87], v[248:251], v[188:191], v[84:87]
	v_pk_max_i16 v51, v51, 0
	ds_read_b128 v[248:251], v121 offset:38912
	ds_read_b128 v[252:255], v121 offset:39936
	s_setprio 0
	s_waitcnt lgkmcnt(6)
	v_mfma_f32_16x16x32_bf16 v[80:83], v[224:227], v[192:195], v[80:83]
	v_pk_max_i16 v52, v52, 0
	v_mfma_f32_16x16x32_bf16 v[76:79], v[228:231], v[192:195], v[76:79]
	v_pk_max_i16 v53, v53, 0
	v_mfma_f32_16x16x32_bf16 v[72:75], v[228:231], v[196:199], v[72:75]
	v_pk_max_i16 v54, v54, 0
	v_mfma_f32_16x16x32_bf16 v[84:87], v[224:227], v[196:199], v[84:87]
	v_pk_max_i16 v55, v55, 0
	s_waitcnt lgkmcnt(4)
	v_mfma_f32_16x16x32_bf16 v[80:83], v[232:235], v[200:203], v[80:83]
	v_mfma_f32_16x16x32_bf16 v[76:79], v[236:239], v[200:203], v[76:79]
	v_mfma_f32_16x16x32_bf16 v[72:75], v[236:239], v[204:207], v[72:75]
	v_mfma_f32_16x16x32_bf16 v[84:87], v[232:235], v[204:207], v[84:87]
	s_add_i32 s50, s50, 0x40000
	v_add_u32_e32 v183, 0x800, v183
	s_add_i32 s52, s52, 1
	s_branch .Lnerf_hid_b0
.Lnerf_head:
	s_waitcnt lgkmcnt(0)
	ds_read_b128 v[224:227], v149 offset:0
	ds_read_b128 v[228:231], v149 offset:1024
	ds_read_b128 v[4:7], v183 offset:1024
	ds_read_b128 v[0:3], v183 offset:1024
	v_mfma_f32_16x16x32_bf16 v[80:83], v[240:243], v[48:51], v[80:83]
	ds_read_b128 v[232:235], v149 offset:2048
	ds_read_b128 v[236:239], v149 offset:3072
	v_mfma_f32_16x16x32_bf16 v[76:79], v[244:247], v[48:51], v[76:79]
	v_mfma_f32_16x16x32_bf16 v[72:75], v[244:247], v[52:55], v[72:75]
	v_mfma_f32_16x16x32_bf16 v[84:87], v[240:243], v[52:55], v[84:87]
	ds_read_b128 v[240:243], v149 offset:4096
	ds_read_b128 v[244:247], v149 offset:5120
	v_mfma_f32_16x16x32_bf16 v[80:83], v[248:251], v[112:115], v[80:83]
	v_mfma_f32_16x16x32_bf16 v[76:79], v[252:255], v[112:115], v[76:79]
	v_mfma_f32_16x16x32_bf16 v[72:75], v[252:255], v[116:119], v[72:75]
	v_mfma_f32_16x16x32_bf16 v[84:87], v[248:251], v[116:119], v[84:87]
	ds_read_b128 v[248:251], v149 offset:6144
	ds_read_b128 v[252:255], v149 offset:7168
	s_waitcnt lgkmcnt(7)
	v_mfma_f32_16x16x32_bf16 v[4:7], v[224:227], v[88:91], v[4:7]
	s_waitcnt lgkmcnt(6)
	v_mfma_f32_16x16x32_bf16 v[0:3], v[224:227], v[92:95], v[0:3]
	v_cvt_pk_bf16_f32 v216, v80, v81
	v_cvt_pk_bf16_f32 v217, v82, v83
	v_mfma_f32_16x16x32_bf16 v[4:7], v[228:231], v[96:99], v[4:7]
	v_cvt_pk_bf16_f32 v218, v76, v77
	v_cvt_pk_bf16_f32 v219, v78, v79
	v_mfma_f32_16x16x32_bf16 v[0:3], v[228:231], v[100:103], v[0:3]
	v_cvt_pk_bf16_f32 v220, v84, v85
	v_cvt_pk_bf16_f32 v221, v86, v87
	s_waitcnt lgkmcnt(5)
	v_mfma_f32_16x16x32_bf16 v[4:7], v[232:235], v[104:107], v[4:7]
	v_cvt_pk_bf16_f32 v222, v72, v73
	v_cvt_pk_bf16_f32 v223, v74, v75
	v_mfma_f32_16x16x32_bf16 v[0:3], v[232:235], v[108:111], v[0:3]
	v_pk_max_i16 v216, v216, 0
	v_pk_max_i16 v217, v217, 0
	s_waitcnt lgkmcnt(4)
	v_mfma_f32_16x16x32_bf16 v[4:7], v[236:239], v[184:187], v[4:7]
	v_pk_max_i16 v218, v218, 0
	v_pk_max_i16 v219, v219, 0
	v_mfma_f32_16x16x32_bf16 v[0:3], v[236:239], v[188:191], v[0:3]
	v_pk_max_i16 v220, v220, 0
	v_pk_max_i16 v221, v221, 0
	s_waitcnt lgkmcnt(3)
	v_mfma_f32_16x16x32_bf16 v[4:7], v[240:243], v[192:195], v[4:7]
	v_pk_max_i16 v222, v222, 0
	v_pk_max_i16 v223, v223, 0
	v_mfma_f32_16x16x32_bf16 v[0:3], v[240:243], v[196:199], v[0:3]
	s_waitcnt lgkmcnt(2)
	v_mfma_f32_16x16x32_bf16 v[4:7], v[244:247], v[200:203], v[4:7]
	v_mfma_f32_16x16x32_bf16 v[0:3], v[244:247], v[204:207], v[0:3]
	s_waitcnt lgkmcnt(1)
	v_mfma_f32_16x16x32_bf16 v[4:7], v[248:251], v[208:211], v[4:7]
	v_mfma_f32_16x16x32_bf16 v[0:3], v[248:251], v[212:215], v[0:3]
	s_nop 1
	s_waitcnt lgkmcnt(0)
	v_mfma_f32_16x16x32_bf16 v[4:7], v[252:255], v[216:219], v[4:7]
	v_mfma_f32_16x16x32_bf16 v[0:3], v[252:255], v[220:223], v[0:3]
	s_setprio 0
	s_and_saveexec_b64 s[20:21], s[2:3]
	s_cbranch_execz .LBB1_20
	s_nop 4
	v_mul_f32_e32 v6, 0xbfb8aa3b, v6
	v_mul_f32_e32 v7, 0xbfb8aa3b, v7
	v_mul_f32_e32 v4, 0xbfb8aa3b, v4
	v_mul_f32_e32 v5, 0xbfb8aa3b, v5
	v_exp_f32_e32 v6, v6
	v_exp_f32_e32 v7, v7
	v_exp_f32_e32 v4, v4
	v_exp_f32_e32 v5, v5
	s_lshl_b32 s24, s45, 6
	s_add_i32 s47, s43, s24
	s_nop 0
	v_add_f32_e32 v6, 1.0, v6
	v_add_f32_e32 v7, 1.0, v7
	v_add_f32_e32 v4, 1.0, v4
	v_add_f32_e32 v5, 1.0, v5
	v_rcp_f32_e32 v6, v6
	v_rcp_f32_e32 v7, v7
	v_rcp_f32_e32 v4, v4
	v_rcp_f32_e32 v5, v5
	s_mov_b64 s[24:25], -1
	s_nop 0
	s_and_b64 vcc, exec, s[16:17]
	s_cbranch_vccz .LBB1_14
	v_or_b32_e32 v8, s47, v130
	v_lshl_add_u32 v8, v8, 4, v182
	ds_write_b128 v8, v[4:7]
	s_mov_b64 s[24:25], 0
